# v57 + code placement: every MFMA block of the three GEMM K-loops (incl. out-proj main loop) on the 4-mod-8 address phase via s_nop pads; downstream code phase unchanged
# speedup vs baseline: 1.0005x; 1.0003x over previous
.LBB0_264:
	s_ashr_i32 s73, s72, 31
	s_lshl_b64 s[26:27], s[72:73], 21
	s_add_u32 s76, s38, s26
	s_addc_u32 s77, s40, s27
	s_and_b64 s[26:27], s[4:5], exec
	s_cselect_b32 s73, s77, s7
	s_cselect_b32 vcc_lo, s76, s6
	s_ashr_i32 s75, s74, 31
	s_lshl_b64 s[26:27], s[74:75], 21
	s_add_u32 s96, s42, s26
	s_addc_u32 s97, s44, s27
	s_and_b64 s[26:27], s[4:5], exec
	s_cselect_b32 s75, s97, s25
	s_cselect_b32 vcc_hi, s96, s24
	s_add_u32 s6, s6, 0x100080
	s_addc_u32 s7, s7, 0
	s_add_u32 s21, s24, 0x100
	s_addc_u32 s13, s25, 0
	s_mov_b32 s58, -2
	s_add_u32 s24, s6, 0xfff00080
	s_addc_u32 s25, s7, -1
	s_add_i32 s28, 0, 0x10000
	s_cmp_eq_u32 s58, 60
	s_cselect_b32 s27, s73, s25
	s_cselect_b32 s26, vcc_lo, s24
	s_cselect_b32 s25, s75, s13
	s_cselect_b32 s24, vcc_hi, s21
	s_add_i32 s71, 0, 0x14000
	v_add_u32_e32 v144, s28, v163
	v_add_u32_e32 v182, s71, v163
	s_waitcnt lgkmcnt(0)
	ds_read_b128 v[132:135], v144
	ds_read_b128 v[136:139], v144 offset:1024
	ds_read_b128 v[140:143], v144 offset:2048
	ds_read_b128 v[144:147], v144 offset:3072
	ds_read_b128 v[148:151], v182
	ds_read_b128 v[152:155], v182 offset:1024
	ds_read_b128 v[178:181], v182 offset:2048
	ds_read_b128 v[186:189], v182 offset:3072
	v_lshl_add_u64 v[182:183], s[6:7], 0, v[174:175]
	s_add_i32 m0, s46, 0xc000
	ds_read_b128 v[190:193], v184
	ds_read_b128 v[194:197], v184 offset:1024
	ds_read_b128 v[198:201], v184 offset:2048
	ds_read_b128 v[202:205], v184 offset:3072
	ds_read_b128 v[222:225], v184 offset:4096
	ds_read_b128 v[226:229], v184 offset:5120
	ds_read_b128 v[230:233], v184 offset:6144
	ds_read_b128 v[234:237], v184 offset:7168
	global_load_lds_dwordx4 v[182:183], off
	v_lshl_add_u64 v[182:183], s[6:7], 0, v[176:177]
	s_add_i32 m0, s46, 0xe000
	s_nop 0
	global_load_lds_dwordx4 v[182:183], off
	s_waitcnt vmcnt(8)
	s_waitcnt lgkmcnt(0)
	s_setprio 1
	s_barrier
	v_mfma_f32_16x16x32_bf16 v[120:123], v[132:135], v[190:193], 0
	v_mfma_f32_16x16x32_bf16 v[116:119], v[140:143], v[190:193], 0
	v_mfma_f32_16x16x32_bf16 v[104:107], v[132:135], v[198:201], 0
	v_mfma_f32_16x16x32_bf16 v[100:103], v[140:143], v[198:201], 0
	v_mfma_f32_16x16x32_bf16 v[88:91], v[132:135], v[222:225], 0
	v_mfma_f32_16x16x32_bf16 v[84:87], v[140:143], v[222:225], 0
	v_mfma_f32_16x16x32_bf16 v[72:75], v[132:135], v[230:233], 0
	v_mfma_f32_16x16x32_bf16 v[68:71], v[140:143], v[230:233], 0
	v_mfma_f32_16x16x32_bf16 v[120:123], v[136:139], v[194:197], v[120:123]
	v_mfma_f32_16x16x32_bf16 v[116:119], v[144:147], v[194:197], v[116:119]
	v_mfma_f32_16x16x32_bf16 v[104:107], v[136:139], v[202:205], v[104:107]
	v_mfma_f32_16x16x32_bf16 v[100:103], v[144:147], v[202:205], v[100:103]
	v_mfma_f32_16x16x32_bf16 v[88:91], v[136:139], v[226:229], v[88:91]
	v_mfma_f32_16x16x32_bf16 v[84:87], v[144:147], v[226:229], v[84:87]
	v_mfma_f32_16x16x32_bf16 v[72:75], v[136:139], v[234:237], v[72:75]
	v_mfma_f32_16x16x32_bf16 v[68:71], v[144:147], v[234:237], v[68:71]
	v_mfma_f32_16x16x32_bf16 v[128:131], v[148:151], v[190:193], 0
	v_mfma_f32_16x16x32_bf16 v[124:127], v[178:181], v[190:193], 0
	v_mfma_f32_16x16x32_bf16 v[112:115], v[148:151], v[198:201], 0
	v_mfma_f32_16x16x32_bf16 v[108:111], v[178:181], v[198:201], 0
	v_mfma_f32_16x16x32_bf16 v[96:99], v[148:151], v[222:225], 0
	v_mfma_f32_16x16x32_bf16 v[92:95], v[178:181], v[222:225], 0
	v_mfma_f32_16x16x32_bf16 v[80:83], v[148:151], v[230:233], 0
	v_mfma_f32_16x16x32_bf16 v[76:79], v[178:181], v[230:233], 0
	v_mfma_f32_16x16x32_bf16 v[128:131], v[152:155], v[194:197], v[128:131]
	v_mfma_f32_16x16x32_bf16 v[124:127], v[186:189], v[194:197], v[124:127]
	v_mfma_f32_16x16x32_bf16 v[112:115], v[152:155], v[202:205], v[112:115]
	v_mfma_f32_16x16x32_bf16 v[108:111], v[186:189], v[202:205], v[108:111]
	v_mfma_f32_16x16x32_bf16 v[96:99], v[152:155], v[226:229], v[96:99]
	v_mfma_f32_16x16x32_bf16 v[92:95], v[186:189], v[226:229], v[92:95]
	v_mfma_f32_16x16x32_bf16 v[80:83], v[152:155], v[234:237], v[80:83]
	v_mfma_f32_16x16x32_bf16 v[76:79], v[186:189], v[234:237], v[76:79]
	s_barrier
	s_setprio 0
	s_add_i32 s28, s28, s1
	v_lshl_add_u64 v[182:183], s[24:25], 0, v[2:3]
	s_mov_b32 m0, s28
	ds_read_b128 v[190:193], v184 offset:16384
	ds_read_b128 v[194:197], v184 offset:17408
	ds_read_b128 v[198:201], v184 offset:18432
	ds_read_b128 v[202:205], v184 offset:19456
	ds_read_b128 v[222:225], v184 offset:20480
	ds_read_b128 v[226:229], v184 offset:21504
	ds_read_b128 v[230:233], v184 offset:22528
	ds_read_b128 v[234:237], v184 offset:23552
	global_load_lds_dwordx4 v[182:183], off
	s_add_i32 m0, s28, 0x2000
	s_add_u32 s28, s24, 0x100000
	v_lshl_add_u64 v[238:239], s[24:25], 0, v[168:169]
	s_addc_u32 s29, s25, 0
	s_add_i32 s71, s71, s1
	global_load_lds_dwordx4 v[238:239], off
	v_lshl_add_u64 v[240:241], s[28:29], 0, v[2:3]
	s_mov_b32 m0, s71
	v_lshl_add_u64 v[242:243], s[26:27], 0, v[170:171]
	global_load_lds_dwordx4 v[240:241], off
	v_lshl_add_u64 v[240:241], s[28:29], 0, v[168:169]
	s_add_i32 m0, s71, 0x2000
	s_nop 0
	global_load_lds_dwordx4 v[240:241], off
	v_lshl_add_u64 v[240:241], s[26:27], 0, v[172:173]
	s_mov_b32 m0, s46
	s_nop 0
	global_load_lds_dwordx4 v[240:241], off
	s_mov_b32 m0, s50
	s_nop 0
	global_load_lds_dwordx4 v[242:243], off
	s_waitcnt vmcnt(8)
	s_waitcnt lgkmcnt(0)
	s_setprio 1
	s_barrier
	v_mfma_f32_16x16x32_bf16 v[56:59], v[132:135], v[190:193], 0
	v_mfma_f32_16x16x32_bf16 v[52:55], v[140:143], v[190:193], 0
	v_mfma_f32_16x16x32_bf16 v[40:43], v[132:135], v[198:201], 0
	v_mfma_f32_16x16x32_bf16 v[36:39], v[140:143], v[198:201], 0
	v_mfma_f32_16x16x32_bf16 v[24:27], v[132:135], v[222:225], 0
	v_mfma_f32_16x16x32_bf16 v[20:23], v[140:143], v[222:225], 0
	v_mfma_f32_16x16x32_bf16 v[8:11], v[132:135], v[230:233], 0
	v_mfma_f32_16x16x32_bf16 v[4:7], v[140:143], v[230:233], 0
	v_mfma_f32_16x16x32_bf16 v[56:59], v[136:139], v[194:197], v[56:59]
	v_mfma_f32_16x16x32_bf16 v[52:55], v[144:147], v[194:197], v[52:55]
	v_mfma_f32_16x16x32_bf16 v[40:43], v[136:139], v[202:205], v[40:43]
	v_mfma_f32_16x16x32_bf16 v[36:39], v[144:147], v[202:205], v[36:39]
	v_mfma_f32_16x16x32_bf16 v[24:27], v[136:139], v[226:229], v[24:27]
	v_mfma_f32_16x16x32_bf16 v[20:23], v[144:147], v[226:229], v[20:23]
	v_mfma_f32_16x16x32_bf16 v[8:11], v[136:139], v[234:237], v[8:11]
	v_mfma_f32_16x16x32_bf16 v[4:7], v[144:147], v[234:237], v[4:7]
	v_mfma_f32_16x16x32_bf16 v[64:67], v[148:151], v[190:193], 0
	v_mfma_f32_16x16x32_bf16 v[60:63], v[178:181], v[190:193], 0
	v_mfma_f32_16x16x32_bf16 v[48:51], v[148:151], v[198:201], 0
	v_mfma_f32_16x16x32_bf16 v[44:47], v[178:181], v[198:201], 0
	v_mfma_f32_16x16x32_bf16 v[32:35], v[148:151], v[222:225], 0
	v_mfma_f32_16x16x32_bf16 v[28:31], v[178:181], v[222:225], 0
	v_mfma_f32_16x16x32_bf16 v[16:19], v[148:151], v[230:233], 0
	v_mfma_f32_16x16x32_bf16 v[12:15], v[178:181], v[230:233], 0
	v_mfma_f32_16x16x32_bf16 v[64:67], v[152:155], v[194:197], v[64:67]
	v_mfma_f32_16x16x32_bf16 v[60:63], v[186:189], v[194:197], v[60:63]
	v_mfma_f32_16x16x32_bf16 v[48:51], v[152:155], v[202:205], v[48:51]
	v_mfma_f32_16x16x32_bf16 v[44:47], v[186:189], v[202:205], v[44:47]
	v_mfma_f32_16x16x32_bf16 v[32:35], v[152:155], v[226:229], v[32:35]
	v_mfma_f32_16x16x32_bf16 v[28:31], v[186:189], v[226:229], v[28:31]
	v_mfma_f32_16x16x32_bf16 v[16:19], v[152:155], v[234:237], v[16:19]
	v_mfma_f32_16x16x32_bf16 v[12:15], v[186:189], v[234:237], v[12:15]
	s_barrier
	s_setprio 0
	s_add_i32 s28, 0, 0x18000
	s_add_i32 s29, 0, 0x1c000
	v_add_u32_e32 v144, s28, v163
	v_add_u32_e32 v185, s29, v163
	ds_read_b128 v[132:135], v144
	ds_read_b128 v[136:139], v144 offset:1024
	ds_read_b128 v[140:143], v144 offset:2048
	ds_read_b128 v[144:147], v144 offset:3072
	ds_read_b128 v[148:151], v185
	ds_read_b128 v[152:155], v185 offset:1024
	ds_read_b128 v[178:181], v185 offset:2048
	ds_read_b128 v[186:189], v185 offset:3072
	s_add_u32 s26, s26, 0x100000
	s_addc_u32 s27, s27, 0
	s_mov_b32 m0, s51
	v_lshl_add_u64 v[244:245], s[26:27], 0, v[172:173]
	ds_read_b128 v[190:193], v184 offset:32768
	ds_read_b128 v[194:197], v184 offset:33792
	ds_read_b128 v[198:201], v184 offset:34816
	ds_read_b128 v[202:205], v184 offset:35840
	ds_read_b128 v[222:225], v184 offset:36864
	ds_read_b128 v[226:229], v184 offset:37888
	ds_read_b128 v[230:233], v184 offset:38912
	ds_read_b128 v[234:237], v184 offset:39936
	global_load_lds_dwordx4 v[244:245], off
	v_lshl_add_u64 v[244:245], s[26:27], 0, v[170:171]
	s_mov_b32 m0, s54
	s_nop 0
	global_load_lds_dwordx4 v[244:245], off
	s_waitcnt vmcnt(8)
	s_waitcnt lgkmcnt(0)
	s_setprio 1
	s_barrier
	v_mfma_f32_16x16x32_bf16 v[120:123], v[132:135], v[190:193], v[120:123]
	v_mfma_f32_16x16x32_bf16 v[116:119], v[140:143], v[190:193], v[116:119]
	v_mfma_f32_16x16x32_bf16 v[104:107], v[132:135], v[198:201], v[104:107]
	v_mfma_f32_16x16x32_bf16 v[100:103], v[140:143], v[198:201], v[100:103]
	v_mfma_f32_16x16x32_bf16 v[88:91], v[132:135], v[222:225], v[88:91]
	v_mfma_f32_16x16x32_bf16 v[84:87], v[140:143], v[222:225], v[84:87]
	v_mfma_f32_16x16x32_bf16 v[72:75], v[132:135], v[230:233], v[72:75]
	v_mfma_f32_16x16x32_bf16 v[68:71], v[140:143], v[230:233], v[68:71]
	v_mfma_f32_16x16x32_bf16 v[120:123], v[136:139], v[194:197], v[120:123]
	v_mfma_f32_16x16x32_bf16 v[116:119], v[144:147], v[194:197], v[116:119]
	v_mfma_f32_16x16x32_bf16 v[104:107], v[136:139], v[202:205], v[104:107]
	v_mfma_f32_16x16x32_bf16 v[100:103], v[144:147], v[202:205], v[100:103]
	v_mfma_f32_16x16x32_bf16 v[88:91], v[136:139], v[226:229], v[88:91]
	v_mfma_f32_16x16x32_bf16 v[84:87], v[144:147], v[226:229], v[84:87]
	v_mfma_f32_16x16x32_bf16 v[72:75], v[136:139], v[234:237], v[72:75]
	v_mfma_f32_16x16x32_bf16 v[68:71], v[144:147], v[234:237], v[68:71]
	v_mfma_f32_16x16x32_bf16 v[128:131], v[148:151], v[190:193], v[128:131]
	v_mfma_f32_16x16x32_bf16 v[124:127], v[178:181], v[190:193], v[124:127]
	v_mfma_f32_16x16x32_bf16 v[112:115], v[148:151], v[198:201], v[112:115]
	v_mfma_f32_16x16x32_bf16 v[108:111], v[178:181], v[198:201], v[108:111]
	v_mfma_f32_16x16x32_bf16 v[96:99], v[148:151], v[222:225], v[96:99]
	v_mfma_f32_16x16x32_bf16 v[92:95], v[178:181], v[222:225], v[92:95]
	v_mfma_f32_16x16x32_bf16 v[80:83], v[148:151], v[230:233], v[80:83]
	v_mfma_f32_16x16x32_bf16 v[76:79], v[178:181], v[230:233], v[76:79]
	v_mfma_f32_16x16x32_bf16 v[128:131], v[152:155], v[194:197], v[128:131]
	v_mfma_f32_16x16x32_bf16 v[124:127], v[186:189], v[194:197], v[124:127]
	v_mfma_f32_16x16x32_bf16 v[112:115], v[152:155], v[202:205], v[112:115]
	v_mfma_f32_16x16x32_bf16 v[108:111], v[186:189], v[202:205], v[108:111]
	v_mfma_f32_16x16x32_bf16 v[96:99], v[152:155], v[226:229], v[96:99]
	v_mfma_f32_16x16x32_bf16 v[92:95], v[186:189], v[226:229], v[92:95]
	v_mfma_f32_16x16x32_bf16 v[80:83], v[152:155], v[234:237], v[80:83]
	v_mfma_f32_16x16x32_bf16 v[76:79], v[186:189], v[234:237], v[76:79]
	s_barrier
	s_setprio 0
	s_add_i32 s26, s28, s1
	v_lshl_add_u64 v[182:183], v[182:183], 0, s[86:87]
	s_mov_b32 m0, s26
	ds_read_b128 v[190:193], v184 offset:49152
	ds_read_b128 v[194:197], v184 offset:50176
	ds_read_b128 v[198:201], v184 offset:51200
	ds_read_b128 v[202:205], v184 offset:52224
	ds_read_b128 v[222:225], v184 offset:53248
	ds_read_b128 v[226:229], v184 offset:54272
	ds_read_b128 v[230:233], v184 offset:55296
	ds_read_b128 v[234:237], v184 offset:56320
	global_load_lds_dwordx4 v[182:183], off
	s_add_i32 m0, s26, 0x2000
	s_add_u32 s24, s24, 0x100080
	v_lshl_add_u64 v[182:183], v[238:239], 0, s[86:87]
	s_addc_u32 s25, s25, 0
	s_add_i32 s26, s29, s1
	global_load_lds_dwordx4 v[182:183], off
	v_lshl_add_u64 v[182:183], s[24:25], 0, v[2:3]
	s_mov_b32 m0, s26
	s_nop 0
	global_load_lds_dwordx4 v[182:183], off
	v_lshl_add_u64 v[182:183], s[24:25], 0, v[168:169]
	s_add_i32 m0, s26, 0x2000
	s_nop 0
	global_load_lds_dwordx4 v[182:183], off
	v_lshl_add_u64 v[182:183], v[240:241], 0, s[86:87]
	s_mov_b32 m0, s78
	s_nop 0
	global_load_lds_dwordx4 v[182:183], off
	v_lshl_add_u64 v[182:183], v[242:243], 0, s[86:87]
	s_mov_b32 m0, s85
	s_nop 0
	global_load_lds_dwordx4 v[182:183], off
	s_waitcnt vmcnt(8)
	s_waitcnt lgkmcnt(0)
	s_nop 0
	s_setprio 1
	s_barrier
	v_mfma_f32_16x16x32_bf16 v[56:59], v[132:135], v[190:193], v[56:59]
	v_mfma_f32_16x16x32_bf16 v[52:55], v[140:143], v[190:193], v[52:55]
	v_mfma_f32_16x16x32_bf16 v[40:43], v[132:135], v[198:201], v[40:43]
	v_mfma_f32_16x16x32_bf16 v[36:39], v[140:143], v[198:201], v[36:39]
	v_mfma_f32_16x16x32_bf16 v[24:27], v[132:135], v[222:225], v[24:27]
	v_mfma_f32_16x16x32_bf16 v[20:23], v[140:143], v[222:225], v[20:23]
	v_mfma_f32_16x16x32_bf16 v[8:11], v[132:135], v[230:233], v[8:11]
	v_mfma_f32_16x16x32_bf16 v[4:7], v[140:143], v[230:233], v[4:7]
	v_mfma_f32_16x16x32_bf16 v[56:59], v[136:139], v[194:197], v[56:59]
	v_mfma_f32_16x16x32_bf16 v[52:55], v[144:147], v[194:197], v[52:55]
	v_mfma_f32_16x16x32_bf16 v[40:43], v[136:139], v[202:205], v[40:43]
	v_mfma_f32_16x16x32_bf16 v[36:39], v[144:147], v[202:205], v[36:39]
	v_mfma_f32_16x16x32_bf16 v[24:27], v[136:139], v[226:229], v[24:27]
	v_mfma_f32_16x16x32_bf16 v[20:23], v[144:147], v[226:229], v[20:23]
	v_mfma_f32_16x16x32_bf16 v[8:11], v[136:139], v[234:237], v[8:11]
	v_mfma_f32_16x16x32_bf16 v[4:7], v[144:147], v[234:237], v[4:7]
	v_mfma_f32_16x16x32_bf16 v[64:67], v[148:151], v[190:193], v[64:67]
	v_mfma_f32_16x16x32_bf16 v[60:63], v[178:181], v[190:193], v[60:63]
	v_mfma_f32_16x16x32_bf16 v[48:51], v[148:151], v[198:201], v[48:51]
	v_mfma_f32_16x16x32_bf16 v[44:47], v[178:181], v[198:201], v[44:47]
	v_mfma_f32_16x16x32_bf16 v[32:35], v[148:151], v[222:225], v[32:35]
	v_mfma_f32_16x16x32_bf16 v[28:31], v[178:181], v[222:225], v[28:31]
	v_mfma_f32_16x16x32_bf16 v[16:19], v[148:151], v[230:233], v[16:19]
	v_mfma_f32_16x16x32_bf16 v[12:15], v[178:181], v[230:233], v[12:15]
	v_mfma_f32_16x16x32_bf16 v[64:67], v[152:155], v[194:197], v[64:67]
	v_mfma_f32_16x16x32_bf16 v[60:63], v[186:189], v[194:197], v[60:63]
	v_mfma_f32_16x16x32_bf16 v[48:51], v[152:155], v[202:205], v[48:51]
	v_mfma_f32_16x16x32_bf16 v[44:47], v[186:189], v[202:205], v[44:47]
	v_mfma_f32_16x16x32_bf16 v[32:35], v[152:155], v[226:229], v[32:35]
	v_mfma_f32_16x16x32_bf16 v[28:31], v[186:189], v[226:229], v[28:31]
	v_mfma_f32_16x16x32_bf16 v[16:19], v[152:155], v[234:237], v[16:19]
	v_mfma_f32_16x16x32_bf16 v[12:15], v[186:189], v[234:237], v[12:15]
	s_barrier
	s_setprio 0
	s_nop 0
	s_add_i32 s58, s58, 2
	s_add_u32 s6, s6, 0x100
	s_addc_u32 s7, s7, 0
	s_add_u32 s21, s21, 0x100
	s_addc_u32 s13, s13, 0
	s_cmp_gt_u32 s58, 61
	s_cbranch_scc0 .LBB0_265
.LBB0_265:
	s_add_u32 s24, s6, 0xfff00080
	s_addc_u32 s25, s7, -1
	s_add_i32 s28, 0, 0x10000
	s_cmp_eq_u32 s58, 60
	s_cselect_b32 s27, s73, s25
	s_cselect_b32 s26, vcc_lo, s24
	s_cselect_b32 s25, s75, s13
	s_cselect_b32 s24, vcc_hi, s21
	s_add_i32 s71, 0, 0x14000
	v_add_u32_e32 v144, s28, v163
	v_add_u32_e32 v182, s71, v163
	s_waitcnt lgkmcnt(0)
	ds_read_b128 v[132:135], v144
	ds_read_b128 v[136:139], v144 offset:1024
	ds_read_b128 v[140:143], v144 offset:2048
	ds_read_b128 v[144:147], v144 offset:3072
	ds_read_b128 v[148:151], v182
	ds_read_b128 v[152:155], v182 offset:1024
	ds_read_b128 v[178:181], v182 offset:2048
	ds_read_b128 v[186:189], v182 offset:3072
	v_lshl_add_u64 v[182:183], s[6:7], 0, v[174:175]
	s_add_i32 m0, s46, 0xc000
	ds_read_b128 v[190:193], v184
	ds_read_b128 v[194:197], v184 offset:1024
	ds_read_b128 v[198:201], v184 offset:2048
	ds_read_b128 v[202:205], v184 offset:3072
	ds_read_b128 v[222:225], v184 offset:4096
	ds_read_b128 v[226:229], v184 offset:5120
	ds_read_b128 v[230:233], v184 offset:6144
	ds_read_b128 v[234:237], v184 offset:7168
	global_load_lds_dwordx4 v[182:183], off
	v_lshl_add_u64 v[182:183], s[6:7], 0, v[176:177]
	s_add_i32 m0, s46, 0xe000
	s_nop 0
	global_load_lds_dwordx4 v[182:183], off
	s_waitcnt vmcnt(8)
	s_waitcnt lgkmcnt(0)
	s_setprio 1
	s_barrier
	v_mfma_f32_16x16x32_bf16 v[120:123], v[132:135], v[190:193], v[120:123]
	v_mfma_f32_16x16x32_bf16 v[116:119], v[140:143], v[190:193], v[116:119]
	v_mfma_f32_16x16x32_bf16 v[104:107], v[132:135], v[198:201], v[104:107]
	v_mfma_f32_16x16x32_bf16 v[100:103], v[140:143], v[198:201], v[100:103]
	v_mfma_f32_16x16x32_bf16 v[88:91], v[132:135], v[222:225], v[88:91]
	v_mfma_f32_16x16x32_bf16 v[84:87], v[140:143], v[222:225], v[84:87]
	v_mfma_f32_16x16x32_bf16 v[72:75], v[132:135], v[230:233], v[72:75]
	v_mfma_f32_16x16x32_bf16 v[68:71], v[140:143], v[230:233], v[68:71]
	v_mfma_f32_16x16x32_bf16 v[120:123], v[136:139], v[194:197], v[120:123]
	v_mfma_f32_16x16x32_bf16 v[116:119], v[144:147], v[194:197], v[116:119]
	v_mfma_f32_16x16x32_bf16 v[104:107], v[136:139], v[202:205], v[104:107]
	v_mfma_f32_16x16x32_bf16 v[100:103], v[144:147], v[202:205], v[100:103]
	v_mfma_f32_16x16x32_bf16 v[88:91], v[136:139], v[226:229], v[88:91]
	v_mfma_f32_16x16x32_bf16 v[84:87], v[144:147], v[226:229], v[84:87]
	v_mfma_f32_16x16x32_bf16 v[72:75], v[136:139], v[234:237], v[72:75]
	v_mfma_f32_16x16x32_bf16 v[68:71], v[144:147], v[234:237], v[68:71]
	v_mfma_f32_16x16x32_bf16 v[128:131], v[148:151], v[190:193], v[128:131]
	v_mfma_f32_16x16x32_bf16 v[124:127], v[178:181], v[190:193], v[124:127]
	v_mfma_f32_16x16x32_bf16 v[112:115], v[148:151], v[198:201], v[112:115]
	v_mfma_f32_16x16x32_bf16 v[108:111], v[178:181], v[198:201], v[108:111]
	v_mfma_f32_16x16x32_bf16 v[96:99], v[148:151], v[222:225], v[96:99]
	v_mfma_f32_16x16x32_bf16 v[92:95], v[178:181], v[222:225], v[92:95]
	v_mfma_f32_16x16x32_bf16 v[80:83], v[148:151], v[230:233], v[80:83]
	v_mfma_f32_16x16x32_bf16 v[76:79], v[178:181], v[230:233], v[76:79]
	v_mfma_f32_16x16x32_bf16 v[128:131], v[152:155], v[194:197], v[128:131]
	v_mfma_f32_16x16x32_bf16 v[124:127], v[186:189], v[194:197], v[124:127]
	v_mfma_f32_16x16x32_bf16 v[112:115], v[152:155], v[202:205], v[112:115]
	v_mfma_f32_16x16x32_bf16 v[108:111], v[186:189], v[202:205], v[108:111]
	v_mfma_f32_16x16x32_bf16 v[96:99], v[152:155], v[226:229], v[96:99]
	v_mfma_f32_16x16x32_bf16 v[92:95], v[186:189], v[226:229], v[92:95]
	v_mfma_f32_16x16x32_bf16 v[80:83], v[152:155], v[234:237], v[80:83]
	v_mfma_f32_16x16x32_bf16 v[76:79], v[186:189], v[234:237], v[76:79]
	s_barrier
	s_setprio 0
	s_add_i32 s28, s28, s1
	v_lshl_add_u64 v[182:183], s[24:25], 0, v[2:3]
	s_mov_b32 m0, s28
	ds_read_b128 v[190:193], v184 offset:16384
	ds_read_b128 v[194:197], v184 offset:17408
	ds_read_b128 v[198:201], v184 offset:18432
	ds_read_b128 v[202:205], v184 offset:19456
	ds_read_b128 v[222:225], v184 offset:20480
	ds_read_b128 v[226:229], v184 offset:21504
	ds_read_b128 v[230:233], v184 offset:22528
	ds_read_b128 v[234:237], v184 offset:23552
	global_load_lds_dwordx4 v[182:183], off
	s_add_i32 m0, s28, 0x2000
	s_add_u32 s28, s24, 0x100000
	v_lshl_add_u64 v[238:239], s[24:25], 0, v[168:169]
	s_addc_u32 s29, s25, 0
	s_add_i32 s71, s71, s1
	global_load_lds_dwordx4 v[238:239], off
	v_lshl_add_u64 v[240:241], s[28:29], 0, v[2:3]
	s_mov_b32 m0, s71
	v_lshl_add_u64 v[242:243], s[26:27], 0, v[170:171]
	global_load_lds_dwordx4 v[240:241], off
	v_lshl_add_u64 v[240:241], s[28:29], 0, v[168:169]
	s_add_i32 m0, s71, 0x2000
	s_nop 0
	global_load_lds_dwordx4 v[240:241], off
	v_lshl_add_u64 v[240:241], s[26:27], 0, v[172:173]
	s_mov_b32 m0, s46
	s_nop 0
	global_load_lds_dwordx4 v[240:241], off
	s_mov_b32 m0, s50
	s_nop 0
	global_load_lds_dwordx4 v[242:243], off
	s_waitcnt vmcnt(8)
	s_waitcnt lgkmcnt(0)
	s_setprio 1
	s_barrier
	v_mfma_f32_16x16x32_bf16 v[56:59], v[132:135], v[190:193], v[56:59]
	v_mfma_f32_16x16x32_bf16 v[52:55], v[140:143], v[190:193], v[52:55]
	v_mfma_f32_16x16x32_bf16 v[40:43], v[132:135], v[198:201], v[40:43]
	v_mfma_f32_16x16x32_bf16 v[36:39], v[140:143], v[198:201], v[36:39]
	v_mfma_f32_16x16x32_bf16 v[24:27], v[132:135], v[222:225], v[24:27]
	v_mfma_f32_16x16x32_bf16 v[20:23], v[140:143], v[222:225], v[20:23]
	v_mfma_f32_16x16x32_bf16 v[8:11], v[132:135], v[230:233], v[8:11]
	v_mfma_f32_16x16x32_bf16 v[4:7], v[140:143], v[230:233], v[4:7]
	v_mfma_f32_16x16x32_bf16 v[56:59], v[136:139], v[194:197], v[56:59]
	v_mfma_f32_16x16x32_bf16 v[52:55], v[144:147], v[194:197], v[52:55]
	v_mfma_f32_16x16x32_bf16 v[40:43], v[136:139], v[202:205], v[40:43]
	v_mfma_f32_16x16x32_bf16 v[36:39], v[144:147], v[202:205], v[36:39]
	v_mfma_f32_16x16x32_bf16 v[24:27], v[136:139], v[226:229], v[24:27]
	v_mfma_f32_16x16x32_bf16 v[20:23], v[144:147], v[226:229], v[20:23]
	v_mfma_f32_16x16x32_bf16 v[8:11], v[136:139], v[234:237], v[8:11]
	v_mfma_f32_16x16x32_bf16 v[4:7], v[144:147], v[234:237], v[4:7]
	v_mfma_f32_16x16x32_bf16 v[64:67], v[148:151], v[190:193], v[64:67]
	v_mfma_f32_16x16x32_bf16 v[60:63], v[178:181], v[190:193], v[60:63]
	v_mfma_f32_16x16x32_bf16 v[48:51], v[148:151], v[198:201], v[48:51]
	v_mfma_f32_16x16x32_bf16 v[44:47], v[178:181], v[198:201], v[44:47]
	v_mfma_f32_16x16x32_bf16 v[32:35], v[148:151], v[222:225], v[32:35]
	v_mfma_f32_16x16x32_bf16 v[28:31], v[178:181], v[222:225], v[28:31]
	v_mfma_f32_16x16x32_bf16 v[16:19], v[148:151], v[230:233], v[16:19]
	v_mfma_f32_16x16x32_bf16 v[12:15], v[178:181], v[230:233], v[12:15]
	v_mfma_f32_16x16x32_bf16 v[64:67], v[152:155], v[194:197], v[64:67]
	v_mfma_f32_16x16x32_bf16 v[60:63], v[186:189], v[194:197], v[60:63]
	v_mfma_f32_16x16x32_bf16 v[48:51], v[152:155], v[202:205], v[48:51]
	v_mfma_f32_16x16x32_bf16 v[44:47], v[186:189], v[202:205], v[44:47]
	v_mfma_f32_16x16x32_bf16 v[32:35], v[152:155], v[226:229], v[32:35]
	v_mfma_f32_16x16x32_bf16 v[28:31], v[186:189], v[226:229], v[28:31]
	v_mfma_f32_16x16x32_bf16 v[16:19], v[152:155], v[234:237], v[16:19]
	v_mfma_f32_16x16x32_bf16 v[12:15], v[186:189], v[234:237], v[12:15]
	s_barrier
	s_setprio 0
	s_add_i32 s28, 0, 0x18000
	s_add_i32 s29, 0, 0x1c000
	v_add_u32_e32 v144, s28, v163
	v_add_u32_e32 v185, s29, v163
	ds_read_b128 v[132:135], v144
	ds_read_b128 v[136:139], v144 offset:1024
	ds_read_b128 v[140:143], v144 offset:2048
	ds_read_b128 v[144:147], v144 offset:3072
	ds_read_b128 v[148:151], v185
	ds_read_b128 v[152:155], v185 offset:1024
	ds_read_b128 v[178:181], v185 offset:2048
	ds_read_b128 v[186:189], v185 offset:3072
	s_add_u32 s26, s26, 0x100000
	s_addc_u32 s27, s27, 0
	s_mov_b32 m0, s51
	v_lshl_add_u64 v[244:245], s[26:27], 0, v[172:173]
	ds_read_b128 v[190:193], v184 offset:32768
	ds_read_b128 v[194:197], v184 offset:33792
	ds_read_b128 v[198:201], v184 offset:34816
	ds_read_b128 v[202:205], v184 offset:35840
	ds_read_b128 v[222:225], v184 offset:36864
	ds_read_b128 v[226:229], v184 offset:37888
	ds_read_b128 v[230:233], v184 offset:38912
	ds_read_b128 v[234:237], v184 offset:39936
	global_load_lds_dwordx4 v[244:245], off
	v_lshl_add_u64 v[244:245], s[26:27], 0, v[170:171]
	s_mov_b32 m0, s54
	s_nop 0
	global_load_lds_dwordx4 v[244:245], off
	s_waitcnt vmcnt(8)
	s_waitcnt lgkmcnt(0)
	s_setprio 1
	s_barrier
	v_mfma_f32_16x16x32_bf16 v[120:123], v[132:135], v[190:193], v[120:123]
	v_mfma_f32_16x16x32_bf16 v[116:119], v[140:143], v[190:193], v[116:119]
	v_mfma_f32_16x16x32_bf16 v[104:107], v[132:135], v[198:201], v[104:107]
	v_mfma_f32_16x16x32_bf16 v[100:103], v[140:143], v[198:201], v[100:103]
	v_mfma_f32_16x16x32_bf16 v[88:91], v[132:135], v[222:225], v[88:91]
	v_mfma_f32_16x16x32_bf16 v[84:87], v[140:143], v[222:225], v[84:87]
	v_mfma_f32_16x16x32_bf16 v[72:75], v[132:135], v[230:233], v[72:75]
	v_mfma_f32_16x16x32_bf16 v[68:71], v[140:143], v[230:233], v[68:71]
	v_mfma_f32_16x16x32_bf16 v[120:123], v[136:139], v[194:197], v[120:123]
	v_mfma_f32_16x16x32_bf16 v[116:119], v[144:147], v[194:197], v[116:119]
	v_mfma_f32_16x16x32_bf16 v[104:107], v[136:139], v[202:205], v[104:107]
	v_mfma_f32_16x16x32_bf16 v[100:103], v[144:147], v[202:205], v[100:103]
	v_mfma_f32_16x16x32_bf16 v[88:91], v[136:139], v[226:229], v[88:91]
	v_mfma_f32_16x16x32_bf16 v[84:87], v[144:147], v[226:229], v[84:87]
	v_mfma_f32_16x16x32_bf16 v[72:75], v[136:139], v[234:237], v[72:75]
	v_mfma_f32_16x16x32_bf16 v[68:71], v[144:147], v[234:237], v[68:71]
	v_mfma_f32_16x16x32_bf16 v[128:131], v[148:151], v[190:193], v[128:131]
	v_mfma_f32_16x16x32_bf16 v[124:127], v[178:181], v[190:193], v[124:127]
	v_mfma_f32_16x16x32_bf16 v[112:115], v[148:151], v[198:201], v[112:115]
	v_mfma_f32_16x16x32_bf16 v[108:111], v[178:181], v[198:201], v[108:111]
	v_mfma_f32_16x16x32_bf16 v[96:99], v[148:151], v[222:225], v[96:99]
	v_mfma_f32_16x16x32_bf16 v[92:95], v[178:181], v[222:225], v[92:95]
	v_mfma_f32_16x16x32_bf16 v[80:83], v[148:151], v[230:233], v[80:83]
	v_mfma_f32_16x16x32_bf16 v[76:79], v[178:181], v[230:233], v[76:79]
	v_mfma_f32_16x16x32_bf16 v[128:131], v[152:155], v[194:197], v[128:131]
	v_mfma_f32_16x16x32_bf16 v[124:127], v[186:189], v[194:197], v[124:127]
	v_mfma_f32_16x16x32_bf16 v[112:115], v[152:155], v[202:205], v[112:115]
	v_mfma_f32_16x16x32_bf16 v[108:111], v[186:189], v[202:205], v[108:111]
	v_mfma_f32_16x16x32_bf16 v[96:99], v[152:155], v[226:229], v[96:99]
	v_mfma_f32_16x16x32_bf16 v[92:95], v[186:189], v[226:229], v[92:95]
	v_mfma_f32_16x16x32_bf16 v[80:83], v[152:155], v[234:237], v[80:83]
	v_mfma_f32_16x16x32_bf16 v[76:79], v[186:189], v[234:237], v[76:79]
	s_barrier
	s_setprio 0
	s_add_i32 s26, s28, s1
	v_lshl_add_u64 v[182:183], v[182:183], 0, s[86:87]
	s_mov_b32 m0, s26
	ds_read_b128 v[190:193], v184 offset:49152
	ds_read_b128 v[194:197], v184 offset:50176
	ds_read_b128 v[198:201], v184 offset:51200
	ds_read_b128 v[202:205], v184 offset:52224
	ds_read_b128 v[222:225], v184 offset:53248
	ds_read_b128 v[226:229], v184 offset:54272
	ds_read_b128 v[230:233], v184 offset:55296
	ds_read_b128 v[234:237], v184 offset:56320
	global_load_lds_dwordx4 v[182:183], off
	s_add_i32 m0, s26, 0x2000
	s_add_u32 s24, s24, 0x100080
	v_lshl_add_u64 v[182:183], v[238:239], 0, s[86:87]
	s_addc_u32 s25, s25, 0
	s_add_i32 s26, s29, s1
	global_load_lds_dwordx4 v[182:183], off
	v_lshl_add_u64 v[182:183], s[24:25], 0, v[2:3]
	s_mov_b32 m0, s26
	s_nop 0
	global_load_lds_dwordx4 v[182:183], off
	v_lshl_add_u64 v[182:183], s[24:25], 0, v[168:169]
	s_add_i32 m0, s26, 0x2000
	s_nop 0
	global_load_lds_dwordx4 v[182:183], off
	v_lshl_add_u64 v[182:183], v[240:241], 0, s[86:87]
	s_mov_b32 m0, s78
	s_nop 0
	global_load_lds_dwordx4 v[182:183], off
	v_lshl_add_u64 v[182:183], v[242:243], 0, s[86:87]
	s_mov_b32 m0, s85
	s_nop 0
	global_load_lds_dwordx4 v[182:183], off
	s_waitcnt vmcnt(8)
	s_waitcnt lgkmcnt(0)
	s_nop 0
	s_setprio 1
	s_barrier
	v_mfma_f32_16x16x32_bf16 v[56:59], v[132:135], v[190:193], v[56:59]
	v_mfma_f32_16x16x32_bf16 v[52:55], v[140:143], v[190:193], v[52:55]
	v_mfma_f32_16x16x32_bf16 v[40:43], v[132:135], v[198:201], v[40:43]
	v_mfma_f32_16x16x32_bf16 v[36:39], v[140:143], v[198:201], v[36:39]
	v_mfma_f32_16x16x32_bf16 v[24:27], v[132:135], v[222:225], v[24:27]
	v_mfma_f32_16x16x32_bf16 v[20:23], v[140:143], v[222:225], v[20:23]
	v_mfma_f32_16x16x32_bf16 v[8:11], v[132:135], v[230:233], v[8:11]
	v_mfma_f32_16x16x32_bf16 v[4:7], v[140:143], v[230:233], v[4:7]
	v_mfma_f32_16x16x32_bf16 v[56:59], v[136:139], v[194:197], v[56:59]
	v_mfma_f32_16x16x32_bf16 v[52:55], v[144:147], v[194:197], v[52:55]
	v_mfma_f32_16x16x32_bf16 v[40:43], v[136:139], v[202:205], v[40:43]
	v_mfma_f32_16x16x32_bf16 v[36:39], v[144:147], v[202:205], v[36:39]
	v_mfma_f32_16x16x32_bf16 v[24:27], v[136:139], v[226:229], v[24:27]
	v_mfma_f32_16x16x32_bf16 v[20:23], v[144:147], v[226:229], v[20:23]
	v_mfma_f32_16x16x32_bf16 v[8:11], v[136:139], v[234:237], v[8:11]
	v_mfma_f32_16x16x32_bf16 v[4:7], v[144:147], v[234:237], v[4:7]
	v_mfma_f32_16x16x32_bf16 v[64:67], v[148:151], v[190:193], v[64:67]
	v_mfma_f32_16x16x32_bf16 v[60:63], v[178:181], v[190:193], v[60:63]
	v_mfma_f32_16x16x32_bf16 v[48:51], v[148:151], v[198:201], v[48:51]
	v_mfma_f32_16x16x32_bf16 v[44:47], v[178:181], v[198:201], v[44:47]
	v_mfma_f32_16x16x32_bf16 v[32:35], v[148:151], v[222:225], v[32:35]
	v_mfma_f32_16x16x32_bf16 v[28:31], v[178:181], v[222:225], v[28:31]
	v_mfma_f32_16x16x32_bf16 v[16:19], v[148:151], v[230:233], v[16:19]
	v_mfma_f32_16x16x32_bf16 v[12:15], v[178:181], v[230:233], v[12:15]
	v_mfma_f32_16x16x32_bf16 v[64:67], v[152:155], v[194:197], v[64:67]
	v_mfma_f32_16x16x32_bf16 v[60:63], v[186:189], v[194:197], v[60:63]
	v_mfma_f32_16x16x32_bf16 v[48:51], v[152:155], v[202:205], v[48:51]
	v_mfma_f32_16x16x32_bf16 v[44:47], v[186:189], v[202:205], v[44:47]
	v_mfma_f32_16x16x32_bf16 v[32:35], v[152:155], v[226:229], v[32:35]
	v_mfma_f32_16x16x32_bf16 v[28:31], v[186:189], v[226:229], v[28:31]
	v_mfma_f32_16x16x32_bf16 v[16:19], v[152:155], v[234:237], v[16:19]
	v_mfma_f32_16x16x32_bf16 v[12:15], v[186:189], v[234:237], v[12:15]
	s_barrier
	s_setprio 0
	s_nop 0
	s_add_i32 s58, s58, 2
	s_add_u32 s6, s6, 0x100
	s_addc_u32 s7, s7, 0
	s_add_u32 s21, s21, 0x100
	s_addc_u32 s13, s13, 0
	s_cmp_gt_u32 s58, 61
	s_cbranch_scc0 .LBB0_265
	s_and_b64 vcc, exec, s[30:31]
	s_cbranch_vccz .LBB0_268
	s_barrier

.LBB0_722:
	s_add_u32 s24, s51, s10
	s_addc_u32 s25, s52, s11
	s_add_u32 s24, s24, 0x2b800100
	s_addc_u32 s25, s25, 0
	s_add_u32 s28, s13, s10
	s_addc_u32 s29, s21, s11
	s_add_i32 s54, 0, 0x10000
	s_cmpk_eq_i32 s10, 0x1f00
	s_cselect_b32 s27, s9, s25
	s_cselect_b32 s26, s8, s24
	v_add_u32_e32 v145, s54, v143
	s_cselect_b32 s25, s7, s29
	s_cselect_b32 s24, s6, s28
	s_add_i32 s55, 0, 0x14000
	ds_read_b128 v[146:149], v145
	ds_read_b128 v[150:153], v145 offset:1024
	ds_read_b128 v[170:173], v145 offset:2048
	ds_read_b128 v[174:177], v145 offset:3072
	v_add_u32_e32 v145, s55, v143
	ds_read_b128 v[178:181], v145
	ds_read_b128 v[182:185], v145 offset:1024
	ds_read_b128 v[186:189], v145 offset:2048
	ds_read_b128 v[190:193], v145 offset:3072
	v_lshl_add_u64 v[154:155], v[138:139], 0, s[10:11]
	s_add_i32 m0, s5, 0xc000
	ds_read_b128 v[194:197], v144
	ds_read_b128 v[198:201], v144 offset:1024
	ds_read_b128 v[202:205], v144 offset:2048
	ds_read_b128 v[222:225], v144 offset:3072
	ds_read_b128 v[226:229], v144 offset:4096
	ds_read_b128 v[230:233], v144 offset:5120
	ds_read_b128 v[234:237], v144 offset:6144
	ds_read_b128 v[238:241], v144 offset:7168
	global_load_lds_dwordx4 v[154:155], off
	v_lshl_add_u64 v[154:155], v[140:141], 0, s[10:11]
	s_add_i32 m0, s5, 0xe000
	s_nop 0
	global_load_lds_dwordx4 v[154:155], off
	s_waitcnt vmcnt(8)
	s_waitcnt lgkmcnt(0)
	s_setprio 1
	s_barrier
	v_mfma_f32_16x16x32_bf16 v[128:131], v[146:149], v[194:197], v[128:131]
	v_mfma_f32_16x16x32_bf16 v[124:127], v[170:173], v[194:197], v[124:127]
	v_mfma_f32_16x16x32_bf16 v[116:119], v[146:149], v[202:205], v[116:119]
	v_mfma_f32_16x16x32_bf16 v[108:111], v[170:173], v[202:205], v[108:111]
	v_mfma_f32_16x16x32_bf16 v[100:103], v[146:149], v[226:229], v[100:103]
	v_mfma_f32_16x16x32_bf16 v[92:95], v[170:173], v[226:229], v[92:95]
	v_mfma_f32_16x16x32_bf16 v[84:87], v[146:149], v[234:237], v[84:87]
	v_mfma_f32_16x16x32_bf16 v[76:79], v[170:173], v[234:237], v[76:79]
	v_mfma_f32_16x16x32_bf16 v[128:131], v[150:153], v[198:201], v[128:131]
	v_mfma_f32_16x16x32_bf16 v[124:127], v[174:177], v[198:201], v[124:127]
	v_mfma_f32_16x16x32_bf16 v[116:119], v[150:153], v[222:225], v[116:119]
	v_mfma_f32_16x16x32_bf16 v[108:111], v[174:177], v[222:225], v[108:111]
	v_mfma_f32_16x16x32_bf16 v[100:103], v[150:153], v[230:233], v[100:103]
	v_mfma_f32_16x16x32_bf16 v[92:95], v[174:177], v[230:233], v[92:95]
	v_mfma_f32_16x16x32_bf16 v[84:87], v[150:153], v[238:241], v[84:87]
	v_mfma_f32_16x16x32_bf16 v[76:79], v[174:177], v[238:241], v[76:79]
	v_mfma_f32_16x16x32_bf16 v[120:123], v[178:181], v[194:197], v[120:123]
	v_mfma_f32_16x16x32_bf16 v[112:115], v[186:189], v[194:197], v[112:115]
	v_mfma_f32_16x16x32_bf16 v[104:107], v[178:181], v[202:205], v[104:107]
	v_mfma_f32_16x16x32_bf16 v[96:99], v[186:189], v[202:205], v[96:99]
	v_mfma_f32_16x16x32_bf16 v[88:91], v[178:181], v[226:229], v[88:91]
	v_mfma_f32_16x16x32_bf16 v[80:83], v[186:189], v[226:229], v[80:83]
	v_mfma_f32_16x16x32_bf16 v[72:75], v[178:181], v[234:237], v[72:75]
	v_mfma_f32_16x16x32_bf16 v[68:71], v[186:189], v[234:237], v[68:71]
	v_mfma_f32_16x16x32_bf16 v[120:123], v[182:185], v[198:201], v[120:123]
	v_mfma_f32_16x16x32_bf16 v[112:115], v[190:193], v[198:201], v[112:115]
	v_mfma_f32_16x16x32_bf16 v[104:107], v[182:185], v[222:225], v[104:107]
	v_mfma_f32_16x16x32_bf16 v[96:99], v[190:193], v[222:225], v[96:99]
	v_mfma_f32_16x16x32_bf16 v[88:91], v[182:185], v[230:233], v[88:91]
	v_mfma_f32_16x16x32_bf16 v[80:83], v[190:193], v[230:233], v[80:83]
	v_mfma_f32_16x16x32_bf16 v[72:75], v[182:185], v[238:241], v[72:75]
	v_mfma_f32_16x16x32_bf16 v[68:71], v[190:193], v[238:241], v[68:71]
	s_barrier
	s_setprio 0
	s_add_i32 s28, s54, s31
	v_lshl_add_u64 v[154:155], s[24:25], 0, v[2:3]
	s_mov_b32 m0, s28
	ds_read_b128 v[194:197], v144 offset:16384
	ds_read_b128 v[198:201], v144 offset:17408
	ds_read_b128 v[202:205], v144 offset:18432
	ds_read_b128 v[222:225], v144 offset:19456
	ds_read_b128 v[226:229], v144 offset:20480
	ds_read_b128 v[230:233], v144 offset:21504
	ds_read_b128 v[234:237], v144 offset:22528
	ds_read_b128 v[238:241], v144 offset:23552
	global_load_lds_dwordx4 v[154:155], off
	s_add_i32 m0, s28, 0x2000
	s_add_u32 s28, s24, 0x100000
	v_lshl_add_u64 v[242:243], s[24:25], 0, v[136:137]
	s_addc_u32 s29, s25, 0
	s_add_i32 s54, s55, s31
	global_load_lds_dwordx4 v[242:243], off
	v_lshl_add_u64 v[244:245], s[28:29], 0, v[2:3]
	s_mov_b32 m0, s54
	v_lshl_add_u64 v[246:247], s[26:27], 0, v[134:135]
	global_load_lds_dwordx4 v[244:245], off
	v_lshl_add_u64 v[244:245], s[28:29], 0, v[136:137]
	s_add_i32 m0, s54, 0x2000
	s_nop 0
	global_load_lds_dwordx4 v[244:245], off
	v_lshl_add_u64 v[244:245], s[26:27], 0, v[132:133]
	s_mov_b32 m0, s5
	s_nop 0
	global_load_lds_dwordx4 v[244:245], off
	s_mov_b32 m0, s35
	s_nop 0
	global_load_lds_dwordx4 v[246:247], off
	s_waitcnt vmcnt(8)
	s_waitcnt lgkmcnt(0)
	s_setprio 1
	s_barrier
	v_mfma_f32_16x16x32_bf16 v[64:67], v[146:149], v[194:197], v[64:67]
	v_mfma_f32_16x16x32_bf16 v[60:63], v[170:173], v[194:197], v[60:63]
	v_mfma_f32_16x16x32_bf16 v[52:55], v[146:149], v[202:205], v[52:55]
	v_mfma_f32_16x16x32_bf16 v[44:47], v[170:173], v[202:205], v[44:47]
	v_mfma_f32_16x16x32_bf16 v[36:39], v[146:149], v[226:229], v[36:39]
	v_mfma_f32_16x16x32_bf16 v[28:31], v[170:173], v[226:229], v[28:31]
	v_mfma_f32_16x16x32_bf16 v[20:23], v[146:149], v[234:237], v[20:23]
	v_mfma_f32_16x16x32_bf16 v[12:15], v[170:173], v[234:237], v[12:15]
	v_mfma_f32_16x16x32_bf16 v[64:67], v[150:153], v[198:201], v[64:67]
	v_mfma_f32_16x16x32_bf16 v[60:63], v[174:177], v[198:201], v[60:63]
	v_mfma_f32_16x16x32_bf16 v[52:55], v[150:153], v[222:225], v[52:55]
	v_mfma_f32_16x16x32_bf16 v[44:47], v[174:177], v[222:225], v[44:47]
	v_mfma_f32_16x16x32_bf16 v[36:39], v[150:153], v[230:233], v[36:39]
	v_mfma_f32_16x16x32_bf16 v[28:31], v[174:177], v[230:233], v[28:31]
	v_mfma_f32_16x16x32_bf16 v[20:23], v[150:153], v[238:241], v[20:23]
	v_mfma_f32_16x16x32_bf16 v[12:15], v[174:177], v[238:241], v[12:15]
	v_mfma_f32_16x16x32_bf16 v[56:59], v[178:181], v[194:197], v[56:59]
	v_mfma_f32_16x16x32_bf16 v[48:51], v[186:189], v[194:197], v[48:51]
	v_mfma_f32_16x16x32_bf16 v[40:43], v[178:181], v[202:205], v[40:43]
	v_mfma_f32_16x16x32_bf16 v[32:35], v[186:189], v[202:205], v[32:35]
	v_mfma_f32_16x16x32_bf16 v[24:27], v[178:181], v[226:229], v[24:27]
	v_mfma_f32_16x16x32_bf16 v[16:19], v[186:189], v[226:229], v[16:19]
	v_mfma_f32_16x16x32_bf16 v[8:11], v[178:181], v[234:237], v[8:11]
	v_mfma_f32_16x16x32_bf16 v[4:7], v[186:189], v[234:237], v[4:7]
	v_mfma_f32_16x16x32_bf16 v[56:59], v[182:185], v[198:201], v[56:59]
	v_mfma_f32_16x16x32_bf16 v[48:51], v[190:193], v[198:201], v[48:51]
	v_mfma_f32_16x16x32_bf16 v[40:43], v[182:185], v[222:225], v[40:43]
	v_mfma_f32_16x16x32_bf16 v[32:35], v[190:193], v[222:225], v[32:35]
	v_mfma_f32_16x16x32_bf16 v[24:27], v[182:185], v[230:233], v[24:27]
	v_mfma_f32_16x16x32_bf16 v[16:19], v[190:193], v[230:233], v[16:19]
	v_mfma_f32_16x16x32_bf16 v[8:11], v[182:185], v[238:241], v[8:11]
	v_mfma_f32_16x16x32_bf16 v[4:7], v[190:193], v[238:241], v[4:7]
	s_barrier
	s_setprio 0
	s_add_i32 s28, 0, 0x18000
	v_add_u32_e32 v145, s28, v143
	s_add_i32 s29, 0, 0x1c000
	ds_read_b128 v[146:149], v145
	ds_read_b128 v[150:153], v145 offset:1024
	ds_read_b128 v[170:173], v145 offset:2048
	ds_read_b128 v[174:177], v145 offset:3072
	v_add_u32_e32 v145, s29, v143
	ds_read_b128 v[178:181], v145
	ds_read_b128 v[182:185], v145 offset:1024
	ds_read_b128 v[186:189], v145 offset:2048
	ds_read_b128 v[190:193], v145 offset:3072
	s_add_u32 s26, s26, 0x100000
	s_addc_u32 s27, s27, 0
	s_mov_b32 m0, s38
	v_lshl_add_u64 v[248:249], s[26:27], 0, v[132:133]
	ds_read_b128 v[194:197], v144 offset:32768
	ds_read_b128 v[198:201], v144 offset:33792
	ds_read_b128 v[202:205], v144 offset:34816
	ds_read_b128 v[222:225], v144 offset:35840
	ds_read_b128 v[226:229], v144 offset:36864
	ds_read_b128 v[230:233], v144 offset:37888
	ds_read_b128 v[234:237], v144 offset:38912
	ds_read_b128 v[238:241], v144 offset:39936
	global_load_lds_dwordx4 v[248:249], off
	v_lshl_add_u64 v[248:249], s[26:27], 0, v[134:135]
	s_mov_b32 m0, s42
	s_nop 0
	global_load_lds_dwordx4 v[248:249], off
	s_waitcnt vmcnt(8)
	s_waitcnt lgkmcnt(0)
	s_setprio 1
	s_barrier
	v_mfma_f32_16x16x32_bf16 v[128:131], v[146:149], v[194:197], v[128:131]
	v_mfma_f32_16x16x32_bf16 v[124:127], v[170:173], v[194:197], v[124:127]
	v_mfma_f32_16x16x32_bf16 v[116:119], v[146:149], v[202:205], v[116:119]
	v_mfma_f32_16x16x32_bf16 v[108:111], v[170:173], v[202:205], v[108:111]
	v_mfma_f32_16x16x32_bf16 v[100:103], v[146:149], v[226:229], v[100:103]
	v_mfma_f32_16x16x32_bf16 v[92:95], v[170:173], v[226:229], v[92:95]
	v_mfma_f32_16x16x32_bf16 v[84:87], v[146:149], v[234:237], v[84:87]
	v_mfma_f32_16x16x32_bf16 v[76:79], v[170:173], v[234:237], v[76:79]
	v_mfma_f32_16x16x32_bf16 v[128:131], v[150:153], v[198:201], v[128:131]
	v_mfma_f32_16x16x32_bf16 v[124:127], v[174:177], v[198:201], v[124:127]
	v_mfma_f32_16x16x32_bf16 v[116:119], v[150:153], v[222:225], v[116:119]
	v_mfma_f32_16x16x32_bf16 v[108:111], v[174:177], v[222:225], v[108:111]
	v_mfma_f32_16x16x32_bf16 v[100:103], v[150:153], v[230:233], v[100:103]
	v_mfma_f32_16x16x32_bf16 v[92:95], v[174:177], v[230:233], v[92:95]
	v_mfma_f32_16x16x32_bf16 v[84:87], v[150:153], v[238:241], v[84:87]
	v_mfma_f32_16x16x32_bf16 v[76:79], v[174:177], v[238:241], v[76:79]
	v_mfma_f32_16x16x32_bf16 v[120:123], v[178:181], v[194:197], v[120:123]
	v_mfma_f32_16x16x32_bf16 v[112:115], v[186:189], v[194:197], v[112:115]
	v_mfma_f32_16x16x32_bf16 v[104:107], v[178:181], v[202:205], v[104:107]
	v_mfma_f32_16x16x32_bf16 v[96:99], v[186:189], v[202:205], v[96:99]
	v_mfma_f32_16x16x32_bf16 v[88:91], v[178:181], v[226:229], v[88:91]
	v_mfma_f32_16x16x32_bf16 v[80:83], v[186:189], v[226:229], v[80:83]
	v_mfma_f32_16x16x32_bf16 v[72:75], v[178:181], v[234:237], v[72:75]
	v_mfma_f32_16x16x32_bf16 v[68:71], v[186:189], v[234:237], v[68:71]
	v_mfma_f32_16x16x32_bf16 v[120:123], v[182:185], v[198:201], v[120:123]
	v_mfma_f32_16x16x32_bf16 v[112:115], v[190:193], v[198:201], v[112:115]
	v_mfma_f32_16x16x32_bf16 v[104:107], v[182:185], v[222:225], v[104:107]
	v_mfma_f32_16x16x32_bf16 v[96:99], v[190:193], v[222:225], v[96:99]
	v_mfma_f32_16x16x32_bf16 v[88:91], v[182:185], v[230:233], v[88:91]
	v_mfma_f32_16x16x32_bf16 v[80:83], v[190:193], v[230:233], v[80:83]
	v_mfma_f32_16x16x32_bf16 v[72:75], v[182:185], v[238:241], v[72:75]
	v_mfma_f32_16x16x32_bf16 v[68:71], v[190:193], v[238:241], v[68:71]
	s_barrier
	s_setprio 0
	s_add_i32 s26, s28, s31
	v_lshl_add_u64 v[154:155], v[154:155], 0, s[86:87]
	s_mov_b32 m0, s26
	ds_read_b128 v[194:197], v144 offset:49152
	ds_read_b128 v[198:201], v144 offset:50176
	ds_read_b128 v[202:205], v144 offset:51200
	ds_read_b128 v[222:225], v144 offset:52224
	ds_read_b128 v[226:229], v144 offset:53248
	ds_read_b128 v[230:233], v144 offset:54272
	ds_read_b128 v[234:237], v144 offset:55296
	ds_read_b128 v[238:241], v144 offset:56320
	global_load_lds_dwordx4 v[154:155], off
	s_add_i32 m0, s26, 0x2000
	s_add_u32 s24, s24, 0x100080
	v_lshl_add_u64 v[154:155], v[242:243], 0, s[86:87]
	s_addc_u32 s25, s25, 0
	s_add_i32 s26, s29, s31
	global_load_lds_dwordx4 v[154:155], off
	v_lshl_add_u64 v[154:155], s[24:25], 0, v[2:3]
	s_mov_b32 m0, s26
	s_nop 0
	global_load_lds_dwordx4 v[154:155], off
	v_lshl_add_u64 v[154:155], s[24:25], 0, v[136:137]
	s_add_i32 m0, s26, 0x2000
	s_nop 0
	global_load_lds_dwordx4 v[154:155], off
	v_lshl_add_u64 v[154:155], v[244:245], 0, s[86:87]
	s_mov_b32 m0, s46
	s_nop 0
	global_load_lds_dwordx4 v[154:155], off
	v_lshl_add_u64 v[154:155], v[246:247], 0, s[86:87]
	s_mov_b32 m0, s50
	s_nop 0
	global_load_lds_dwordx4 v[154:155], off
	s_waitcnt vmcnt(8)
	s_waitcnt lgkmcnt(0)
	s_nop 0
	s_setprio 1
	s_barrier
	v_mfma_f32_16x16x32_bf16 v[64:67], v[146:149], v[194:197], v[64:67]
	v_mfma_f32_16x16x32_bf16 v[60:63], v[170:173], v[194:197], v[60:63]
	v_mfma_f32_16x16x32_bf16 v[52:55], v[146:149], v[202:205], v[52:55]
	v_mfma_f32_16x16x32_bf16 v[44:47], v[170:173], v[202:205], v[44:47]
	v_mfma_f32_16x16x32_bf16 v[36:39], v[146:149], v[226:229], v[36:39]
	v_mfma_f32_16x16x32_bf16 v[28:31], v[170:173], v[226:229], v[28:31]
	v_mfma_f32_16x16x32_bf16 v[20:23], v[146:149], v[234:237], v[20:23]
	v_mfma_f32_16x16x32_bf16 v[12:15], v[170:173], v[234:237], v[12:15]
	v_mfma_f32_16x16x32_bf16 v[64:67], v[150:153], v[198:201], v[64:67]
	v_mfma_f32_16x16x32_bf16 v[60:63], v[174:177], v[198:201], v[60:63]
	v_mfma_f32_16x16x32_bf16 v[52:55], v[150:153], v[222:225], v[52:55]
	v_mfma_f32_16x16x32_bf16 v[44:47], v[174:177], v[222:225], v[44:47]
	v_mfma_f32_16x16x32_bf16 v[36:39], v[150:153], v[230:233], v[36:39]
	v_mfma_f32_16x16x32_bf16 v[28:31], v[174:177], v[230:233], v[28:31]
	v_mfma_f32_16x16x32_bf16 v[20:23], v[150:153], v[238:241], v[20:23]
	v_mfma_f32_16x16x32_bf16 v[12:15], v[174:177], v[238:241], v[12:15]
	v_mfma_f32_16x16x32_bf16 v[56:59], v[178:181], v[194:197], v[56:59]
	v_mfma_f32_16x16x32_bf16 v[48:51], v[186:189], v[194:197], v[48:51]
	v_mfma_f32_16x16x32_bf16 v[40:43], v[178:181], v[202:205], v[40:43]
	v_mfma_f32_16x16x32_bf16 v[32:35], v[186:189], v[202:205], v[32:35]
	v_mfma_f32_16x16x32_bf16 v[24:27], v[178:181], v[226:229], v[24:27]
	v_mfma_f32_16x16x32_bf16 v[16:19], v[186:189], v[226:229], v[16:19]
	v_mfma_f32_16x16x32_bf16 v[8:11], v[178:181], v[234:237], v[8:11]
	v_mfma_f32_16x16x32_bf16 v[4:7], v[186:189], v[234:237], v[4:7]
	v_mfma_f32_16x16x32_bf16 v[56:59], v[182:185], v[198:201], v[56:59]
	v_mfma_f32_16x16x32_bf16 v[48:51], v[190:193], v[198:201], v[48:51]
	v_mfma_f32_16x16x32_bf16 v[40:43], v[182:185], v[222:225], v[40:43]
	v_mfma_f32_16x16x32_bf16 v[32:35], v[190:193], v[222:225], v[32:35]
	v_mfma_f32_16x16x32_bf16 v[24:27], v[182:185], v[230:233], v[24:27]
	v_mfma_f32_16x16x32_bf16 v[16:19], v[190:193], v[230:233], v[16:19]
	v_mfma_f32_16x16x32_bf16 v[8:11], v[182:185], v[238:241], v[8:11]
	v_mfma_f32_16x16x32_bf16 v[4:7], v[190:193], v[238:241], v[4:7]
	s_barrier
	s_setprio 0
	s_nop 0
	s_add_i32 s53, s53, 2
	s_add_u32 s10, s10, 0x100
	s_addc_u32 s11, s11, 0
	s_cmp_gt_u32 s53, 61
	s_cbranch_scc0 .LBB0_722
	s_cmpk_lt_u32 s23, 0x100
	s_cbranch_scc0 .LBB0_725
	s_barrier

.LBB0_1201:
	s_ashr_i32 s53, s52, 31
	s_lshl_b64 s[26:27], s[52:53], 21
	s_add_u32 s72, s38, s26
	s_addc_u32 s73, s40, s27
	s_and_b64 s[26:27], s[4:5], exec
	s_cselect_b32 s35, s73, s7
	s_cselect_b32 s53, s72, s6
	s_ashr_i32 s31, s30, 31
	s_lshl_b64 s[26:27], s[30:31], 21
	s_add_u32 s74, s42, s26
	s_addc_u32 s75, s44, s27
	s_and_b64 s[26:27], s[4:5], exec
	s_cselect_b32 s31, s75, s25
	s_cselect_b32 s92, s74, s24
	s_add_u32 s6, s6, 0x100080
	s_addc_u32 s7, s7, 0
	s_add_u32 s21, s24, 0x100
	s_addc_u32 s13, s25, 0
	s_mov_b32 s58, -2
	s_waitcnt lgkmcnt(0)
	s_add_u32 s24, s6, 0xfff00080
	s_addc_u32 s25, s7, -1
	s_add_i32 s28, 0, 0x10000
	s_cmp_eq_u32 s58, 60
	s_cselect_b32 s27, s35, s25
	s_cselect_b32 s26, s53, s24
	s_cselect_b32 s25, s31, s13
	s_cselect_b32 s24, s92, s21
	s_add_i32 s71, 0, 0x14000
	v_add_u32_e32 v150, s28, v163
	v_add_u32_e32 v154, s71, v163
	ds_read_b128 v[138:141], v150
	ds_read_b128 v[142:145], v150 offset:1024
	ds_read_b128 v[146:149], v150 offset:2048
	ds_read_b128 v[150:153], v150 offset:3072
	ds_read_b128 v[168:171], v154
	ds_read_b128 v[172:175], v154 offset:1024
	ds_read_b128 v[176:179], v154 offset:2048
	ds_read_b128 v[180:183], v154 offset:3072
	v_lshl_add_u64 v[154:155], s[6:7], 0, v[134:135]
	s_add_i32 m0, s50, 0xc000
	ds_read_b128 v[188:191], v186
	ds_read_b128 v[192:195], v186 offset:1024
	ds_read_b128 v[196:199], v186 offset:2048
	ds_read_b128 v[200:203], v186 offset:3072
	ds_read_b128 v[222:225], v186 offset:4096
	ds_read_b128 v[226:229], v186 offset:5120
	ds_read_b128 v[230:233], v186 offset:6144
	ds_read_b128 v[234:237], v186 offset:7168
	global_load_lds_dwordx4 v[154:155], off
	v_lshl_add_u64 v[154:155], s[6:7], 0, v[136:137]
	s_add_i32 m0, s50, 0xe000
	s_nop 0
	global_load_lds_dwordx4 v[154:155], off
	s_waitcnt vmcnt(8)
	s_waitcnt lgkmcnt(0)
	s_setprio 1
	s_barrier
	v_mfma_f32_16x16x32_bf16 v[128:131], v[138:141], v[188:191], 0
	v_mfma_f32_16x16x32_bf16 v[124:127], v[146:149], v[188:191], 0
	v_mfma_f32_16x16x32_bf16 v[112:115], v[138:141], v[196:199], 0
	v_mfma_f32_16x16x32_bf16 v[108:111], v[146:149], v[196:199], 0
	v_mfma_f32_16x16x32_bf16 v[96:99], v[138:141], v[222:225], 0
	v_mfma_f32_16x16x32_bf16 v[92:95], v[146:149], v[222:225], 0
	v_mfma_f32_16x16x32_bf16 v[80:83], v[138:141], v[230:233], 0
	v_mfma_f32_16x16x32_bf16 v[76:79], v[146:149], v[230:233], 0
	v_mfma_f32_16x16x32_bf16 v[128:131], v[142:145], v[192:195], v[128:131]
	v_mfma_f32_16x16x32_bf16 v[124:127], v[150:153], v[192:195], v[124:127]
	v_mfma_f32_16x16x32_bf16 v[112:115], v[142:145], v[200:203], v[112:115]
	v_mfma_f32_16x16x32_bf16 v[108:111], v[150:153], v[200:203], v[108:111]
	v_mfma_f32_16x16x32_bf16 v[96:99], v[142:145], v[226:229], v[96:99]
	v_mfma_f32_16x16x32_bf16 v[92:95], v[150:153], v[226:229], v[92:95]
	v_mfma_f32_16x16x32_bf16 v[80:83], v[142:145], v[234:237], v[80:83]
	v_mfma_f32_16x16x32_bf16 v[76:79], v[150:153], v[234:237], v[76:79]
	v_mfma_f32_16x16x32_bf16 v[120:123], v[168:171], v[188:191], 0
	v_mfma_f32_16x16x32_bf16 v[116:119], v[176:179], v[188:191], 0
	v_mfma_f32_16x16x32_bf16 v[104:107], v[168:171], v[196:199], 0
	v_mfma_f32_16x16x32_bf16 v[100:103], v[176:179], v[196:199], 0
	v_mfma_f32_16x16x32_bf16 v[88:91], v[168:171], v[222:225], 0
	v_mfma_f32_16x16x32_bf16 v[84:87], v[176:179], v[222:225], 0
	v_mfma_f32_16x16x32_bf16 v[72:75], v[168:171], v[230:233], 0
	v_mfma_f32_16x16x32_bf16 v[68:71], v[176:179], v[230:233], 0
	v_mfma_f32_16x16x32_bf16 v[120:123], v[172:175], v[192:195], v[120:123]
	v_mfma_f32_16x16x32_bf16 v[116:119], v[180:183], v[192:195], v[116:119]
	v_mfma_f32_16x16x32_bf16 v[104:107], v[172:175], v[200:203], v[104:107]
	v_mfma_f32_16x16x32_bf16 v[100:103], v[180:183], v[200:203], v[100:103]
	v_mfma_f32_16x16x32_bf16 v[88:91], v[172:175], v[226:229], v[88:91]
	v_mfma_f32_16x16x32_bf16 v[84:87], v[180:183], v[226:229], v[84:87]
	v_mfma_f32_16x16x32_bf16 v[72:75], v[172:175], v[234:237], v[72:75]
	v_mfma_f32_16x16x32_bf16 v[68:71], v[180:183], v[234:237], v[68:71]
	s_barrier
	s_setprio 0
	s_add_i32 s28, s28, s46
	v_lshl_add_u64 v[154:155], s[24:25], 0, v[2:3]
	s_mov_b32 m0, s28
	ds_read_b128 v[188:191], v186 offset:16384
	ds_read_b128 v[192:195], v186 offset:17408
	ds_read_b128 v[196:199], v186 offset:18432
	ds_read_b128 v[200:203], v186 offset:19456
	ds_read_b128 v[222:225], v186 offset:20480
	ds_read_b128 v[226:229], v186 offset:21504
	ds_read_b128 v[230:233], v186 offset:22528
	ds_read_b128 v[234:237], v186 offset:23552
	global_load_lds_dwordx4 v[154:155], off
	s_add_i32 m0, s28, 0x2000
	s_add_u32 s28, s24, 0x100000
	v_lshl_add_u64 v[184:185], s[24:25], 0, v[132:133]
	s_addc_u32 s29, s25, 0
	s_add_i32 s71, s71, s46
	global_load_lds_dwordx4 v[184:185], off
	v_lshl_add_u64 v[204:205], s[28:29], 0, v[2:3]
	s_mov_b32 m0, s71
	v_lshl_add_u64 v[238:239], s[26:27], 0, v[132:133]
	global_load_lds_dwordx4 v[204:205], off
	v_lshl_add_u64 v[204:205], s[28:29], 0, v[132:133]
	s_add_i32 m0, s71, 0x2000
	s_nop 0
	global_load_lds_dwordx4 v[204:205], off
	v_lshl_add_u64 v[204:205], s[26:27], 0, v[2:3]
	s_mov_b32 m0, s50
	s_nop 0
	global_load_lds_dwordx4 v[204:205], off
	s_mov_b32 m0, s23
	s_nop 0
	global_load_lds_dwordx4 v[238:239], off
	s_waitcnt vmcnt(8)
	s_waitcnt lgkmcnt(0)
	s_setprio 1
	s_barrier
	v_mfma_f32_16x16x32_bf16 v[64:67], v[138:141], v[188:191], 0
	v_mfma_f32_16x16x32_bf16 v[60:63], v[146:149], v[188:191], 0
	v_mfma_f32_16x16x32_bf16 v[48:51], v[138:141], v[196:199], 0
	v_mfma_f32_16x16x32_bf16 v[44:47], v[146:149], v[196:199], 0
	v_mfma_f32_16x16x32_bf16 v[32:35], v[138:141], v[222:225], 0
	v_mfma_f32_16x16x32_bf16 v[28:31], v[146:149], v[222:225], 0
	v_mfma_f32_16x16x32_bf16 v[16:19], v[138:141], v[230:233], 0
	v_mfma_f32_16x16x32_bf16 v[12:15], v[146:149], v[230:233], 0
	v_mfma_f32_16x16x32_bf16 v[64:67], v[142:145], v[192:195], v[64:67]
	v_mfma_f32_16x16x32_bf16 v[60:63], v[150:153], v[192:195], v[60:63]
	v_mfma_f32_16x16x32_bf16 v[48:51], v[142:145], v[200:203], v[48:51]
	v_mfma_f32_16x16x32_bf16 v[44:47], v[150:153], v[200:203], v[44:47]
	v_mfma_f32_16x16x32_bf16 v[32:35], v[142:145], v[226:229], v[32:35]
	v_mfma_f32_16x16x32_bf16 v[28:31], v[150:153], v[226:229], v[28:31]
	v_mfma_f32_16x16x32_bf16 v[16:19], v[142:145], v[234:237], v[16:19]
	v_mfma_f32_16x16x32_bf16 v[12:15], v[150:153], v[234:237], v[12:15]
	v_mfma_f32_16x16x32_bf16 v[56:59], v[168:171], v[188:191], 0
	v_mfma_f32_16x16x32_bf16 v[52:55], v[176:179], v[188:191], 0
	v_mfma_f32_16x16x32_bf16 v[40:43], v[168:171], v[196:199], 0
	v_mfma_f32_16x16x32_bf16 v[36:39], v[176:179], v[196:199], 0
	v_mfma_f32_16x16x32_bf16 v[24:27], v[168:171], v[222:225], 0
	v_mfma_f32_16x16x32_bf16 v[20:23], v[176:179], v[222:225], 0
	v_mfma_f32_16x16x32_bf16 v[8:11], v[168:171], v[230:233], 0
	v_mfma_f32_16x16x32_bf16 v[4:7], v[176:179], v[230:233], 0
	v_mfma_f32_16x16x32_bf16 v[56:59], v[172:175], v[192:195], v[56:59]
	v_mfma_f32_16x16x32_bf16 v[52:55], v[180:183], v[192:195], v[52:55]
	v_mfma_f32_16x16x32_bf16 v[40:43], v[172:175], v[200:203], v[40:43]
	v_mfma_f32_16x16x32_bf16 v[36:39], v[180:183], v[200:203], v[36:39]
	v_mfma_f32_16x16x32_bf16 v[24:27], v[172:175], v[226:229], v[24:27]
	v_mfma_f32_16x16x32_bf16 v[20:23], v[180:183], v[226:229], v[20:23]
	v_mfma_f32_16x16x32_bf16 v[8:11], v[172:175], v[234:237], v[8:11]
	v_mfma_f32_16x16x32_bf16 v[4:7], v[180:183], v[234:237], v[4:7]
	s_barrier
	s_setprio 0
	s_add_i32 s28, 0, 0x18000
	s_add_i32 s29, 0, 0x1c000
	v_add_u32_e32 v150, s28, v163
	v_add_u32_e32 v180, s29, v163
	ds_read_b128 v[138:141], v150
	ds_read_b128 v[142:145], v150 offset:1024
	ds_read_b128 v[146:149], v150 offset:2048
	ds_read_b128 v[150:153], v150 offset:3072
	ds_read_b128 v[168:171], v180
	ds_read_b128 v[172:175], v180 offset:1024
	ds_read_b128 v[176:179], v180 offset:2048
	ds_read_b128 v[180:183], v180 offset:3072
	s_add_u32 s26, s26, 0x100000
	s_addc_u32 s27, s27, 0
	s_mov_b32 m0, s51
	v_lshl_add_u64 v[240:241], s[26:27], 0, v[2:3]
	ds_read_b128 v[188:191], v186 offset:32768
	ds_read_b128 v[192:195], v186 offset:33792
	ds_read_b128 v[196:199], v186 offset:34816
	ds_read_b128 v[200:203], v186 offset:35840
	ds_read_b128 v[222:225], v186 offset:36864
	ds_read_b128 v[226:229], v186 offset:37888
	ds_read_b128 v[230:233], v186 offset:38912
	ds_read_b128 v[234:237], v186 offset:39936
	global_load_lds_dwordx4 v[240:241], off
	v_lshl_add_u64 v[240:241], s[26:27], 0, v[132:133]
	s_mov_b32 m0, s54
	s_nop 0
	global_load_lds_dwordx4 v[240:241], off
	s_waitcnt vmcnt(8)
	s_waitcnt lgkmcnt(0)
	s_setprio 1
	s_barrier
	v_mfma_f32_16x16x32_bf16 v[128:131], v[138:141], v[188:191], v[128:131]
	v_mfma_f32_16x16x32_bf16 v[124:127], v[146:149], v[188:191], v[124:127]
	v_mfma_f32_16x16x32_bf16 v[112:115], v[138:141], v[196:199], v[112:115]
	v_mfma_f32_16x16x32_bf16 v[108:111], v[146:149], v[196:199], v[108:111]
	v_mfma_f32_16x16x32_bf16 v[96:99], v[138:141], v[222:225], v[96:99]
	v_mfma_f32_16x16x32_bf16 v[92:95], v[146:149], v[222:225], v[92:95]
	v_mfma_f32_16x16x32_bf16 v[80:83], v[138:141], v[230:233], v[80:83]
	v_mfma_f32_16x16x32_bf16 v[76:79], v[146:149], v[230:233], v[76:79]
	v_mfma_f32_16x16x32_bf16 v[128:131], v[142:145], v[192:195], v[128:131]
	v_mfma_f32_16x16x32_bf16 v[124:127], v[150:153], v[192:195], v[124:127]
	v_mfma_f32_16x16x32_bf16 v[112:115], v[142:145], v[200:203], v[112:115]
	v_mfma_f32_16x16x32_bf16 v[108:111], v[150:153], v[200:203], v[108:111]
	v_mfma_f32_16x16x32_bf16 v[96:99], v[142:145], v[226:229], v[96:99]
	v_mfma_f32_16x16x32_bf16 v[92:95], v[150:153], v[226:229], v[92:95]
	v_mfma_f32_16x16x32_bf16 v[80:83], v[142:145], v[234:237], v[80:83]
	v_mfma_f32_16x16x32_bf16 v[76:79], v[150:153], v[234:237], v[76:79]
	v_mfma_f32_16x16x32_bf16 v[120:123], v[168:171], v[188:191], v[120:123]
	v_mfma_f32_16x16x32_bf16 v[116:119], v[176:179], v[188:191], v[116:119]
	v_mfma_f32_16x16x32_bf16 v[104:107], v[168:171], v[196:199], v[104:107]
	v_mfma_f32_16x16x32_bf16 v[100:103], v[176:179], v[196:199], v[100:103]
	v_mfma_f32_16x16x32_bf16 v[88:91], v[168:171], v[222:225], v[88:91]
	v_mfma_f32_16x16x32_bf16 v[84:87], v[176:179], v[222:225], v[84:87]
	v_mfma_f32_16x16x32_bf16 v[72:75], v[168:171], v[230:233], v[72:75]
	v_mfma_f32_16x16x32_bf16 v[68:71], v[176:179], v[230:233], v[68:71]
	v_mfma_f32_16x16x32_bf16 v[120:123], v[172:175], v[192:195], v[120:123]
	v_mfma_f32_16x16x32_bf16 v[116:119], v[180:183], v[192:195], v[116:119]
	v_mfma_f32_16x16x32_bf16 v[104:107], v[172:175], v[200:203], v[104:107]
	v_mfma_f32_16x16x32_bf16 v[100:103], v[180:183], v[200:203], v[100:103]
	v_mfma_f32_16x16x32_bf16 v[88:91], v[172:175], v[226:229], v[88:91]
	v_mfma_f32_16x16x32_bf16 v[84:87], v[180:183], v[226:229], v[84:87]
	v_mfma_f32_16x16x32_bf16 v[72:75], v[172:175], v[234:237], v[72:75]
	v_mfma_f32_16x16x32_bf16 v[68:71], v[180:183], v[234:237], v[68:71]
	s_barrier
	s_setprio 0
	s_add_i32 s26, s28, s46
	v_lshl_add_u64 v[154:155], v[154:155], 0, s[86:87]
	s_mov_b32 m0, s26
	ds_read_b128 v[188:191], v186 offset:49152
	ds_read_b128 v[192:195], v186 offset:50176
	ds_read_b128 v[196:199], v186 offset:51200
	ds_read_b128 v[200:203], v186 offset:52224
	ds_read_b128 v[222:225], v186 offset:53248
	ds_read_b128 v[226:229], v186 offset:54272
	ds_read_b128 v[230:233], v186 offset:55296
	ds_read_b128 v[234:237], v186 offset:56320
	global_load_lds_dwordx4 v[154:155], off
	s_add_i32 m0, s26, 0x2000
	s_add_u32 s24, s24, 0x100080
	v_lshl_add_u64 v[154:155], v[184:185], 0, s[86:87]
	s_addc_u32 s25, s25, 0
	s_add_i32 s26, s29, s46
	global_load_lds_dwordx4 v[154:155], off
	v_lshl_add_u64 v[154:155], s[24:25], 0, v[2:3]
	s_mov_b32 m0, s26
	s_nop 0
	global_load_lds_dwordx4 v[154:155], off
	v_lshl_add_u64 v[154:155], s[24:25], 0, v[132:133]
	s_add_i32 m0, s26, 0x2000
	s_nop 0
	global_load_lds_dwordx4 v[154:155], off
	v_lshl_add_u64 v[154:155], v[204:205], 0, s[86:87]
	s_mov_b32 m0, s76
	s_nop 0
	global_load_lds_dwordx4 v[154:155], off
	v_lshl_add_u64 v[154:155], v[238:239], 0, s[86:87]
	s_mov_b32 m0, s77
	s_nop 0
	global_load_lds_dwordx4 v[154:155], off
	s_waitcnt vmcnt(8)
	s_waitcnt lgkmcnt(0)
	s_nop 0
	s_setprio 1
	s_barrier
	v_mfma_f32_16x16x32_bf16 v[64:67], v[138:141], v[188:191], v[64:67]
	v_mfma_f32_16x16x32_bf16 v[60:63], v[146:149], v[188:191], v[60:63]
	v_mfma_f32_16x16x32_bf16 v[48:51], v[138:141], v[196:199], v[48:51]
	v_mfma_f32_16x16x32_bf16 v[44:47], v[146:149], v[196:199], v[44:47]
	v_mfma_f32_16x16x32_bf16 v[32:35], v[138:141], v[222:225], v[32:35]
	v_mfma_f32_16x16x32_bf16 v[28:31], v[146:149], v[222:225], v[28:31]
	v_mfma_f32_16x16x32_bf16 v[16:19], v[138:141], v[230:233], v[16:19]
	v_mfma_f32_16x16x32_bf16 v[12:15], v[146:149], v[230:233], v[12:15]
	v_mfma_f32_16x16x32_bf16 v[64:67], v[142:145], v[192:195], v[64:67]
	v_mfma_f32_16x16x32_bf16 v[60:63], v[150:153], v[192:195], v[60:63]
	v_mfma_f32_16x16x32_bf16 v[48:51], v[142:145], v[200:203], v[48:51]
	v_mfma_f32_16x16x32_bf16 v[44:47], v[150:153], v[200:203], v[44:47]
	v_mfma_f32_16x16x32_bf16 v[32:35], v[142:145], v[226:229], v[32:35]
	v_mfma_f32_16x16x32_bf16 v[28:31], v[150:153], v[226:229], v[28:31]
	v_mfma_f32_16x16x32_bf16 v[16:19], v[142:145], v[234:237], v[16:19]
	v_mfma_f32_16x16x32_bf16 v[12:15], v[150:153], v[234:237], v[12:15]
	v_mfma_f32_16x16x32_bf16 v[56:59], v[168:171], v[188:191], v[56:59]
	v_mfma_f32_16x16x32_bf16 v[52:55], v[176:179], v[188:191], v[52:55]
	v_mfma_f32_16x16x32_bf16 v[40:43], v[168:171], v[196:199], v[40:43]
	v_mfma_f32_16x16x32_bf16 v[36:39], v[176:179], v[196:199], v[36:39]
	v_mfma_f32_16x16x32_bf16 v[24:27], v[168:171], v[222:225], v[24:27]
	v_mfma_f32_16x16x32_bf16 v[20:23], v[176:179], v[222:225], v[20:23]
	v_mfma_f32_16x16x32_bf16 v[8:11], v[168:171], v[230:233], v[8:11]
	v_mfma_f32_16x16x32_bf16 v[4:7], v[176:179], v[230:233], v[4:7]
	v_mfma_f32_16x16x32_bf16 v[56:59], v[172:175], v[192:195], v[56:59]
	v_mfma_f32_16x16x32_bf16 v[52:55], v[180:183], v[192:195], v[52:55]
	v_mfma_f32_16x16x32_bf16 v[40:43], v[172:175], v[200:203], v[40:43]
	v_mfma_f32_16x16x32_bf16 v[36:39], v[180:183], v[200:203], v[36:39]
	v_mfma_f32_16x16x32_bf16 v[24:27], v[172:175], v[226:229], v[24:27]
	v_mfma_f32_16x16x32_bf16 v[20:23], v[180:183], v[226:229], v[20:23]
	v_mfma_f32_16x16x32_bf16 v[8:11], v[172:175], v[234:237], v[8:11]
	v_mfma_f32_16x16x32_bf16 v[4:7], v[180:183], v[234:237], v[4:7]
	s_barrier
	s_setprio 0
	s_nop 0
	s_add_i32 s58, s58, 2
	s_add_u32 s6, s6, 0x100
	s_addc_u32 s7, s7, 0
	s_add_u32 s21, s21, 0x100
	s_addc_u32 s13, s13, 0
	s_cmp_gt_u32 s58, 61
	s_cbranch_scc0 .LBB0_1202
	s_nop 0
.LBB0_1202:
	s_add_u32 s24, s6, 0xfff00080
	s_addc_u32 s25, s7, -1
	s_add_i32 s28, 0, 0x10000
	s_cmp_eq_u32 s58, 60
	s_cselect_b32 s27, s35, s25
	s_cselect_b32 s26, s53, s24
	s_cselect_b32 s25, s31, s13
	s_cselect_b32 s24, s92, s21
	s_add_i32 s71, 0, 0x14000
	v_add_u32_e32 v150, s28, v163
	v_add_u32_e32 v154, s71, v163
	ds_read_b128 v[138:141], v150
	ds_read_b128 v[142:145], v150 offset:1024
	ds_read_b128 v[146:149], v150 offset:2048
	ds_read_b128 v[150:153], v150 offset:3072
	ds_read_b128 v[168:171], v154
	ds_read_b128 v[172:175], v154 offset:1024
	ds_read_b128 v[176:179], v154 offset:2048
	ds_read_b128 v[180:183], v154 offset:3072
	v_lshl_add_u64 v[154:155], s[6:7], 0, v[134:135]
	s_add_i32 m0, s50, 0xc000
	ds_read_b128 v[188:191], v186
	ds_read_b128 v[192:195], v186 offset:1024
	ds_read_b128 v[196:199], v186 offset:2048
	ds_read_b128 v[200:203], v186 offset:3072
	ds_read_b128 v[222:225], v186 offset:4096
	ds_read_b128 v[226:229], v186 offset:5120
	ds_read_b128 v[230:233], v186 offset:6144
	ds_read_b128 v[234:237], v186 offset:7168
	global_load_lds_dwordx4 v[154:155], off
	v_lshl_add_u64 v[154:155], s[6:7], 0, v[136:137]
	s_add_i32 m0, s50, 0xe000
	s_nop 0
	global_load_lds_dwordx4 v[154:155], off
	s_waitcnt vmcnt(8)
	s_waitcnt lgkmcnt(0)
	s_setprio 1
	s_barrier
	v_mfma_f32_16x16x32_bf16 v[128:131], v[138:141], v[188:191], v[128:131]
	v_mfma_f32_16x16x32_bf16 v[124:127], v[146:149], v[188:191], v[124:127]
	v_mfma_f32_16x16x32_bf16 v[112:115], v[138:141], v[196:199], v[112:115]
	v_mfma_f32_16x16x32_bf16 v[108:111], v[146:149], v[196:199], v[108:111]
	v_mfma_f32_16x16x32_bf16 v[96:99], v[138:141], v[222:225], v[96:99]
	v_mfma_f32_16x16x32_bf16 v[92:95], v[146:149], v[222:225], v[92:95]
	v_mfma_f32_16x16x32_bf16 v[80:83], v[138:141], v[230:233], v[80:83]
	v_mfma_f32_16x16x32_bf16 v[76:79], v[146:149], v[230:233], v[76:79]
	v_mfma_f32_16x16x32_bf16 v[128:131], v[142:145], v[192:195], v[128:131]
	v_mfma_f32_16x16x32_bf16 v[124:127], v[150:153], v[192:195], v[124:127]
	v_mfma_f32_16x16x32_bf16 v[112:115], v[142:145], v[200:203], v[112:115]
	v_mfma_f32_16x16x32_bf16 v[108:111], v[150:153], v[200:203], v[108:111]
	v_mfma_f32_16x16x32_bf16 v[96:99], v[142:145], v[226:229], v[96:99]
	v_mfma_f32_16x16x32_bf16 v[92:95], v[150:153], v[226:229], v[92:95]
	v_mfma_f32_16x16x32_bf16 v[80:83], v[142:145], v[234:237], v[80:83]
	v_mfma_f32_16x16x32_bf16 v[76:79], v[150:153], v[234:237], v[76:79]
	v_mfma_f32_16x16x32_bf16 v[120:123], v[168:171], v[188:191], v[120:123]
	v_mfma_f32_16x16x32_bf16 v[116:119], v[176:179], v[188:191], v[116:119]
	v_mfma_f32_16x16x32_bf16 v[104:107], v[168:171], v[196:199], v[104:107]
	v_mfma_f32_16x16x32_bf16 v[100:103], v[176:179], v[196:199], v[100:103]
	v_mfma_f32_16x16x32_bf16 v[88:91], v[168:171], v[222:225], v[88:91]
	v_mfma_f32_16x16x32_bf16 v[84:87], v[176:179], v[222:225], v[84:87]
	v_mfma_f32_16x16x32_bf16 v[72:75], v[168:171], v[230:233], v[72:75]
	v_mfma_f32_16x16x32_bf16 v[68:71], v[176:179], v[230:233], v[68:71]
	v_mfma_f32_16x16x32_bf16 v[120:123], v[172:175], v[192:195], v[120:123]
	v_mfma_f32_16x16x32_bf16 v[116:119], v[180:183], v[192:195], v[116:119]
	v_mfma_f32_16x16x32_bf16 v[104:107], v[172:175], v[200:203], v[104:107]
	v_mfma_f32_16x16x32_bf16 v[100:103], v[180:183], v[200:203], v[100:103]
	v_mfma_f32_16x16x32_bf16 v[88:91], v[172:175], v[226:229], v[88:91]
	v_mfma_f32_16x16x32_bf16 v[84:87], v[180:183], v[226:229], v[84:87]
	v_mfma_f32_16x16x32_bf16 v[72:75], v[172:175], v[234:237], v[72:75]
	v_mfma_f32_16x16x32_bf16 v[68:71], v[180:183], v[234:237], v[68:71]
	s_barrier
	s_setprio 0
	s_add_i32 s28, s28, s46
	v_lshl_add_u64 v[154:155], s[24:25], 0, v[2:3]
	s_mov_b32 m0, s28
	ds_read_b128 v[188:191], v186 offset:16384
	ds_read_b128 v[192:195], v186 offset:17408
	ds_read_b128 v[196:199], v186 offset:18432
	ds_read_b128 v[200:203], v186 offset:19456
	ds_read_b128 v[222:225], v186 offset:20480
	ds_read_b128 v[226:229], v186 offset:21504
	ds_read_b128 v[230:233], v186 offset:22528
	ds_read_b128 v[234:237], v186 offset:23552
	global_load_lds_dwordx4 v[154:155], off
	s_add_i32 m0, s28, 0x2000
	s_add_u32 s28, s24, 0x100000
	v_lshl_add_u64 v[184:185], s[24:25], 0, v[132:133]
	s_addc_u32 s29, s25, 0
	s_add_i32 s71, s71, s46
	global_load_lds_dwordx4 v[184:185], off
	v_lshl_add_u64 v[204:205], s[28:29], 0, v[2:3]
	s_mov_b32 m0, s71
	v_lshl_add_u64 v[238:239], s[26:27], 0, v[132:133]
	global_load_lds_dwordx4 v[204:205], off
	v_lshl_add_u64 v[204:205], s[28:29], 0, v[132:133]
	s_add_i32 m0, s71, 0x2000
	s_nop 0
	global_load_lds_dwordx4 v[204:205], off
	v_lshl_add_u64 v[204:205], s[26:27], 0, v[2:3]
	s_mov_b32 m0, s50
	s_nop 0
	global_load_lds_dwordx4 v[204:205], off
	s_mov_b32 m0, s23
	s_nop 0
	global_load_lds_dwordx4 v[238:239], off
	s_waitcnt vmcnt(8)
	s_waitcnt lgkmcnt(0)
	s_setprio 1
	s_barrier
	v_mfma_f32_16x16x32_bf16 v[64:67], v[138:141], v[188:191], v[64:67]
	v_mfma_f32_16x16x32_bf16 v[60:63], v[146:149], v[188:191], v[60:63]
	v_mfma_f32_16x16x32_bf16 v[48:51], v[138:141], v[196:199], v[48:51]
	v_mfma_f32_16x16x32_bf16 v[44:47], v[146:149], v[196:199], v[44:47]
	v_mfma_f32_16x16x32_bf16 v[32:35], v[138:141], v[222:225], v[32:35]
	v_mfma_f32_16x16x32_bf16 v[28:31], v[146:149], v[222:225], v[28:31]
	v_mfma_f32_16x16x32_bf16 v[16:19], v[138:141], v[230:233], v[16:19]
	v_mfma_f32_16x16x32_bf16 v[12:15], v[146:149], v[230:233], v[12:15]
	v_mfma_f32_16x16x32_bf16 v[64:67], v[142:145], v[192:195], v[64:67]
	v_mfma_f32_16x16x32_bf16 v[60:63], v[150:153], v[192:195], v[60:63]
	v_mfma_f32_16x16x32_bf16 v[48:51], v[142:145], v[200:203], v[48:51]
	v_mfma_f32_16x16x32_bf16 v[44:47], v[150:153], v[200:203], v[44:47]
	v_mfma_f32_16x16x32_bf16 v[32:35], v[142:145], v[226:229], v[32:35]
	v_mfma_f32_16x16x32_bf16 v[28:31], v[150:153], v[226:229], v[28:31]
	v_mfma_f32_16x16x32_bf16 v[16:19], v[142:145], v[234:237], v[16:19]
	v_mfma_f32_16x16x32_bf16 v[12:15], v[150:153], v[234:237], v[12:15]
	v_mfma_f32_16x16x32_bf16 v[56:59], v[168:171], v[188:191], v[56:59]
	v_mfma_f32_16x16x32_bf16 v[52:55], v[176:179], v[188:191], v[52:55]
	v_mfma_f32_16x16x32_bf16 v[40:43], v[168:171], v[196:199], v[40:43]
	v_mfma_f32_16x16x32_bf16 v[36:39], v[176:179], v[196:199], v[36:39]
	v_mfma_f32_16x16x32_bf16 v[24:27], v[168:171], v[222:225], v[24:27]
	v_mfma_f32_16x16x32_bf16 v[20:23], v[176:179], v[222:225], v[20:23]
	v_mfma_f32_16x16x32_bf16 v[8:11], v[168:171], v[230:233], v[8:11]
	v_mfma_f32_16x16x32_bf16 v[4:7], v[176:179], v[230:233], v[4:7]
	v_mfma_f32_16x16x32_bf16 v[56:59], v[172:175], v[192:195], v[56:59]
	v_mfma_f32_16x16x32_bf16 v[52:55], v[180:183], v[192:195], v[52:55]
	v_mfma_f32_16x16x32_bf16 v[40:43], v[172:175], v[200:203], v[40:43]
	v_mfma_f32_16x16x32_bf16 v[36:39], v[180:183], v[200:203], v[36:39]
	v_mfma_f32_16x16x32_bf16 v[24:27], v[172:175], v[226:229], v[24:27]
	v_mfma_f32_16x16x32_bf16 v[20:23], v[180:183], v[226:229], v[20:23]
	v_mfma_f32_16x16x32_bf16 v[8:11], v[172:175], v[234:237], v[8:11]
	v_mfma_f32_16x16x32_bf16 v[4:7], v[180:183], v[234:237], v[4:7]
	s_barrier
	s_setprio 0
	s_add_i32 s28, 0, 0x18000
	s_add_i32 s29, 0, 0x1c000
	v_add_u32_e32 v150, s28, v163
	v_add_u32_e32 v180, s29, v163
	ds_read_b128 v[138:141], v150
	ds_read_b128 v[142:145], v150 offset:1024
	ds_read_b128 v[146:149], v150 offset:2048
	ds_read_b128 v[150:153], v150 offset:3072
	ds_read_b128 v[168:171], v180
	ds_read_b128 v[172:175], v180 offset:1024
	ds_read_b128 v[176:179], v180 offset:2048
	ds_read_b128 v[180:183], v180 offset:3072
	s_add_u32 s26, s26, 0x100000
	s_addc_u32 s27, s27, 0
	s_mov_b32 m0, s51
	v_lshl_add_u64 v[240:241], s[26:27], 0, v[2:3]
	ds_read_b128 v[188:191], v186 offset:32768
	ds_read_b128 v[192:195], v186 offset:33792
	ds_read_b128 v[196:199], v186 offset:34816
	ds_read_b128 v[200:203], v186 offset:35840
	ds_read_b128 v[222:225], v186 offset:36864
	ds_read_b128 v[226:229], v186 offset:37888
	ds_read_b128 v[230:233], v186 offset:38912
	ds_read_b128 v[234:237], v186 offset:39936
	global_load_lds_dwordx4 v[240:241], off
	v_lshl_add_u64 v[240:241], s[26:27], 0, v[132:133]
	s_mov_b32 m0, s54
	s_nop 0
	global_load_lds_dwordx4 v[240:241], off
	s_waitcnt vmcnt(8)
	s_waitcnt lgkmcnt(0)
	s_setprio 1
	s_barrier
	v_mfma_f32_16x16x32_bf16 v[128:131], v[138:141], v[188:191], v[128:131]
	v_mfma_f32_16x16x32_bf16 v[124:127], v[146:149], v[188:191], v[124:127]
	v_mfma_f32_16x16x32_bf16 v[112:115], v[138:141], v[196:199], v[112:115]
	v_mfma_f32_16x16x32_bf16 v[108:111], v[146:149], v[196:199], v[108:111]
	v_mfma_f32_16x16x32_bf16 v[96:99], v[138:141], v[222:225], v[96:99]
	v_mfma_f32_16x16x32_bf16 v[92:95], v[146:149], v[222:225], v[92:95]
	v_mfma_f32_16x16x32_bf16 v[80:83], v[138:141], v[230:233], v[80:83]
	v_mfma_f32_16x16x32_bf16 v[76:79], v[146:149], v[230:233], v[76:79]
	v_mfma_f32_16x16x32_bf16 v[128:131], v[142:145], v[192:195], v[128:131]
	v_mfma_f32_16x16x32_bf16 v[124:127], v[150:153], v[192:195], v[124:127]
	v_mfma_f32_16x16x32_bf16 v[112:115], v[142:145], v[200:203], v[112:115]
	v_mfma_f32_16x16x32_bf16 v[108:111], v[150:153], v[200:203], v[108:111]
	v_mfma_f32_16x16x32_bf16 v[96:99], v[142:145], v[226:229], v[96:99]
	v_mfma_f32_16x16x32_bf16 v[92:95], v[150:153], v[226:229], v[92:95]
	v_mfma_f32_16x16x32_bf16 v[80:83], v[142:145], v[234:237], v[80:83]
	v_mfma_f32_16x16x32_bf16 v[76:79], v[150:153], v[234:237], v[76:79]
	v_mfma_f32_16x16x32_bf16 v[120:123], v[168:171], v[188:191], v[120:123]
	v_mfma_f32_16x16x32_bf16 v[116:119], v[176:179], v[188:191], v[116:119]
	v_mfma_f32_16x16x32_bf16 v[104:107], v[168:171], v[196:199], v[104:107]
	v_mfma_f32_16x16x32_bf16 v[100:103], v[176:179], v[196:199], v[100:103]
	v_mfma_f32_16x16x32_bf16 v[88:91], v[168:171], v[222:225], v[88:91]
	v_mfma_f32_16x16x32_bf16 v[84:87], v[176:179], v[222:225], v[84:87]
	v_mfma_f32_16x16x32_bf16 v[72:75], v[168:171], v[230:233], v[72:75]
	v_mfma_f32_16x16x32_bf16 v[68:71], v[176:179], v[230:233], v[68:71]
	v_mfma_f32_16x16x32_bf16 v[120:123], v[172:175], v[192:195], v[120:123]
	v_mfma_f32_16x16x32_bf16 v[116:119], v[180:183], v[192:195], v[116:119]
	v_mfma_f32_16x16x32_bf16 v[104:107], v[172:175], v[200:203], v[104:107]
	v_mfma_f32_16x16x32_bf16 v[100:103], v[180:183], v[200:203], v[100:103]
	v_mfma_f32_16x16x32_bf16 v[88:91], v[172:175], v[226:229], v[88:91]
	v_mfma_f32_16x16x32_bf16 v[84:87], v[180:183], v[226:229], v[84:87]
	v_mfma_f32_16x16x32_bf16 v[72:75], v[172:175], v[234:237], v[72:75]
	v_mfma_f32_16x16x32_bf16 v[68:71], v[180:183], v[234:237], v[68:71]
	s_barrier
	s_setprio 0
	s_add_i32 s26, s28, s46
	v_lshl_add_u64 v[154:155], v[154:155], 0, s[86:87]
	s_mov_b32 m0, s26
	ds_read_b128 v[188:191], v186 offset:49152
	ds_read_b128 v[192:195], v186 offset:50176
	ds_read_b128 v[196:199], v186 offset:51200
	ds_read_b128 v[200:203], v186 offset:52224
	ds_read_b128 v[222:225], v186 offset:53248
	ds_read_b128 v[226:229], v186 offset:54272
	ds_read_b128 v[230:233], v186 offset:55296
	ds_read_b128 v[234:237], v186 offset:56320
	global_load_lds_dwordx4 v[154:155], off
	s_add_i32 m0, s26, 0x2000
	s_add_u32 s24, s24, 0x100080
	v_lshl_add_u64 v[154:155], v[184:185], 0, s[86:87]
	s_addc_u32 s25, s25, 0
	s_add_i32 s26, s29, s46
	global_load_lds_dwordx4 v[154:155], off
	v_lshl_add_u64 v[154:155], s[24:25], 0, v[2:3]
	s_mov_b32 m0, s26
	s_nop 0
	global_load_lds_dwordx4 v[154:155], off
	v_lshl_add_u64 v[154:155], s[24:25], 0, v[132:133]
	s_add_i32 m0, s26, 0x2000
	s_nop 0
	global_load_lds_dwordx4 v[154:155], off
	v_lshl_add_u64 v[154:155], v[204:205], 0, s[86:87]
	s_mov_b32 m0, s76
	s_nop 0
	global_load_lds_dwordx4 v[154:155], off
	v_lshl_add_u64 v[154:155], v[238:239], 0, s[86:87]
	s_mov_b32 m0, s77
	s_nop 0
	global_load_lds_dwordx4 v[154:155], off
	s_waitcnt vmcnt(8)
	s_waitcnt lgkmcnt(0)
	s_nop 0
	s_setprio 1
	s_barrier
	v_mfma_f32_16x16x32_bf16 v[64:67], v[138:141], v[188:191], v[64:67]
	v_mfma_f32_16x16x32_bf16 v[60:63], v[146:149], v[188:191], v[60:63]
	v_mfma_f32_16x16x32_bf16 v[48:51], v[138:141], v[196:199], v[48:51]
	v_mfma_f32_16x16x32_bf16 v[44:47], v[146:149], v[196:199], v[44:47]
	v_mfma_f32_16x16x32_bf16 v[32:35], v[138:141], v[222:225], v[32:35]
	v_mfma_f32_16x16x32_bf16 v[28:31], v[146:149], v[222:225], v[28:31]
	v_mfma_f32_16x16x32_bf16 v[16:19], v[138:141], v[230:233], v[16:19]
	v_mfma_f32_16x16x32_bf16 v[12:15], v[146:149], v[230:233], v[12:15]
	v_mfma_f32_16x16x32_bf16 v[64:67], v[142:145], v[192:195], v[64:67]
	v_mfma_f32_16x16x32_bf16 v[60:63], v[150:153], v[192:195], v[60:63]
	v_mfma_f32_16x16x32_bf16 v[48:51], v[142:145], v[200:203], v[48:51]
	v_mfma_f32_16x16x32_bf16 v[44:47], v[150:153], v[200:203], v[44:47]
	v_mfma_f32_16x16x32_bf16 v[32:35], v[142:145], v[226:229], v[32:35]
	v_mfma_f32_16x16x32_bf16 v[28:31], v[150:153], v[226:229], v[28:31]
	v_mfma_f32_16x16x32_bf16 v[16:19], v[142:145], v[234:237], v[16:19]
	v_mfma_f32_16x16x32_bf16 v[12:15], v[150:153], v[234:237], v[12:15]
	v_mfma_f32_16x16x32_bf16 v[56:59], v[168:171], v[188:191], v[56:59]
	v_mfma_f32_16x16x32_bf16 v[52:55], v[176:179], v[188:191], v[52:55]
	v_mfma_f32_16x16x32_bf16 v[40:43], v[168:171], v[196:199], v[40:43]
	v_mfma_f32_16x16x32_bf16 v[36:39], v[176:179], v[196:199], v[36:39]
	v_mfma_f32_16x16x32_bf16 v[24:27], v[168:171], v[222:225], v[24:27]
	v_mfma_f32_16x16x32_bf16 v[20:23], v[176:179], v[222:225], v[20:23]
	v_mfma_f32_16x16x32_bf16 v[8:11], v[168:171], v[230:233], v[8:11]
	v_mfma_f32_16x16x32_bf16 v[4:7], v[176:179], v[230:233], v[4:7]
	v_mfma_f32_16x16x32_bf16 v[56:59], v[172:175], v[192:195], v[56:59]
	v_mfma_f32_16x16x32_bf16 v[52:55], v[180:183], v[192:195], v[52:55]
	v_mfma_f32_16x16x32_bf16 v[40:43], v[172:175], v[200:203], v[40:43]
	v_mfma_f32_16x16x32_bf16 v[36:39], v[180:183], v[200:203], v[36:39]
	v_mfma_f32_16x16x32_bf16 v[24:27], v[172:175], v[226:229], v[24:27]
	v_mfma_f32_16x16x32_bf16 v[20:23], v[180:183], v[226:229], v[20:23]
	v_mfma_f32_16x16x32_bf16 v[8:11], v[172:175], v[234:237], v[8:11]
	v_mfma_f32_16x16x32_bf16 v[4:7], v[180:183], v[234:237], v[4:7]
	s_barrier
	s_setprio 0
	s_nop 0
	s_add_i32 s58, s58, 2
	s_add_u32 s6, s6, 0x100
	s_addc_u32 s7, s7, 0
	s_add_u32 s21, s21, 0x100
	s_addc_u32 s13, s13, 0
	s_cmp_gt_u32 s58, 61
	s_cbranch_scc0 .LBB0_1202
	s_nop 0
	s_and_b64 vcc, exec, s[14:15]
	s_cbranch_vccz .LBB0_1205
	s_barrier
